# baseline (speedup 1.0000x reference)
.Lex_skip:
.LBB5_148:
	s_or_b32 s2, s49, s28
	s_lshl_b32 s0, s2, 12
	s_mov_b32 s1, 0
	v_lshl_add_u64 v[176:177], v[166:167], 0, s[0:1]
	s_waitcnt vmcnt(0)
	s_waitcnt vmcnt(0) lgkmcnt(0)
	s_barrier
	global_load_dwordx4 v[162:165], v[176:177], off
	global_load_dwordx4 v[168:171], v[176:177], off offset:1024
	global_load_dwordx4 v[172:175], v[176:177], off offset:2048
	s_nop 0
	global_load_dwordx4 v[176:179], v[176:177], off offset:3072
	v_lshl_add_u32 v208, s51, 10, v191
	ds_read_b128 v[192:195], v208
	ds_read_b128 v[196:199], v208 offset:16384
	ds_read_b128 v[200:203], v208 offset:32768
	ds_read_b128 v[204:207], v208 offset:49152
	s_setprio 1
	s_waitcnt lgkmcnt(3)
	v_mfma_f32_16x16x32_f16 v[34:37], v[2:5], v[192:195], v[34:37]
	v_mfma_f32_16x16x32_f16 v[38:41], v[6:9], v[192:195], v[38:41]
	v_mfma_f32_16x16x32_f16 v[42:45], v[10:13], v[192:195], v[42:45]
	v_mfma_f32_16x16x32_f16 v[46:49], v[14:17], v[192:195], v[46:49]
	s_waitcnt lgkmcnt(2)
	v_mfma_f32_16x16x32_f16 v[50:53], v[2:5], v[196:199], v[50:53]
	v_mfma_f32_16x16x32_f16 v[54:57], v[6:9], v[196:199], v[54:57]
	v_mfma_f32_16x16x32_f16 v[58:61], v[10:13], v[196:199], v[58:61]
	v_mfma_f32_16x16x32_f16 v[62:65], v[14:17], v[196:199], v[62:65]
	s_waitcnt lgkmcnt(1)
	v_mfma_f32_16x16x32_f16 v[66:69], v[2:5], v[200:203], v[66:69]
	v_mfma_f32_16x16x32_f16 v[70:73], v[6:9], v[200:203], v[70:73]
	v_mfma_f32_16x16x32_f16 v[74:77], v[10:13], v[200:203], v[74:77]
	v_mfma_f32_16x16x32_f16 v[78:81], v[14:17], v[200:203], v[78:81]
	s_waitcnt lgkmcnt(0)
	v_mfma_f32_16x16x32_f16 v[82:85], v[2:5], v[204:207], v[82:85]
	v_mfma_f32_16x16x32_f16 v[86:89], v[6:9], v[204:207], v[86:89]
	v_mfma_f32_16x16x32_f16 v[90:93], v[10:13], v[204:207], v[90:93]
	v_mfma_f32_16x16x32_f16 v[94:97], v[14:17], v[204:207], v[94:97]
	s_setprio 0
	v_add_u32_e32 v192, 0x10000, v208
	v_add_u32_e32 v196, 0x14000, v208
	v_add_u32_e32 v200, 0x18000, v208
	v_add_u32_e32 v204, 0x1c000, v208
	ds_read_b128 v[192:195], v192
	ds_read_b128 v[196:199], v196
	ds_read_b128 v[200:203], v200
	ds_read_b128 v[204:207], v204
	s_setprio 1
	s_waitcnt lgkmcnt(3)
	v_mfma_f32_16x16x32_f16 v[98:101], v[2:5], v[192:195], v[98:101]
	v_mfma_f32_16x16x32_f16 v[102:105], v[6:9], v[192:195], v[102:105]
	v_mfma_f32_16x16x32_f16 v[106:109], v[10:13], v[192:195], v[106:109]
	v_mfma_f32_16x16x32_f16 v[110:113], v[14:17], v[192:195], v[110:113]
	s_waitcnt lgkmcnt(2)
	v_mfma_f32_16x16x32_f16 v[114:117], v[2:5], v[196:199], v[114:117]
	v_mfma_f32_16x16x32_f16 v[118:121], v[6:9], v[196:199], v[118:121]
	v_mfma_f32_16x16x32_f16 v[122:125], v[10:13], v[196:199], v[122:125]
	v_mfma_f32_16x16x32_f16 v[126:129], v[14:17], v[196:199], v[126:129]
	s_waitcnt lgkmcnt(1)
	v_mfma_f32_16x16x32_f16 v[130:133], v[2:5], v[200:203], v[130:133]
	v_mfma_f32_16x16x32_f16 v[134:137], v[6:9], v[200:203], v[134:137]
	v_mfma_f32_16x16x32_f16 v[138:141], v[10:13], v[200:203], v[138:141]
	v_mfma_f32_16x16x32_f16 v[142:145], v[14:17], v[200:203], v[142:145]
	s_waitcnt lgkmcnt(0)
	v_mfma_f32_16x16x32_f16 v[2:5], v[2:5], v[204:207], v[146:149]
	v_mfma_f32_16x16x32_f16 v[6:9], v[6:9], v[204:207], v[150:153]
	v_mfma_f32_16x16x32_f16 v[10:13], v[10:13], v[204:207], v[154:157]
	v_mfma_f32_16x16x32_f16 v[14:17], v[14:17], v[204:207], v[158:161]
	s_setprio 0
	s_or_b32 s3, s49, s29
	s_lshl_b32 s0, s3, 12
	v_lshl_add_u64 v[158:159], v[166:167], 0, s[0:1]
	global_load_dwordx4 v[146:149], v[158:159], off
	global_load_dwordx4 v[150:153], v[158:159], off offset:1024
	global_load_dwordx4 v[154:157], v[158:159], off offset:2048
	s_nop 0
	global_load_dwordx4 v[158:161], v[158:159], off offset:3072
	v_lshl_add_u32 v208, s52, 10, v191
	ds_read_b128 v[192:195], v208
	ds_read_b128 v[196:199], v208 offset:16384
	ds_read_b128 v[200:203], v208 offset:32768
	ds_read_b128 v[204:207], v208 offset:49152
	s_setprio 1
	s_waitcnt lgkmcnt(3)
	v_mfma_f32_16x16x32_f16 v[34:37], v[18:21], v[192:195], v[34:37]
	v_mfma_f32_16x16x32_f16 v[38:41], v[22:25], v[192:195], v[38:41]
	v_mfma_f32_16x16x32_f16 v[42:45], v[26:29], v[192:195], v[42:45]
	v_mfma_f32_16x16x32_f16 v[46:49], v[30:33], v[192:195], v[46:49]
	s_waitcnt lgkmcnt(2)
	v_mfma_f32_16x16x32_f16 v[50:53], v[18:21], v[196:199], v[50:53]
	v_mfma_f32_16x16x32_f16 v[54:57], v[22:25], v[196:199], v[54:57]
	v_mfma_f32_16x16x32_f16 v[58:61], v[26:29], v[196:199], v[58:61]
	v_mfma_f32_16x16x32_f16 v[62:65], v[30:33], v[196:199], v[62:65]
	s_waitcnt lgkmcnt(1)
	v_mfma_f32_16x16x32_f16 v[66:69], v[18:21], v[200:203], v[66:69]
	v_mfma_f32_16x16x32_f16 v[70:73], v[22:25], v[200:203], v[70:73]
	v_mfma_f32_16x16x32_f16 v[74:77], v[26:29], v[200:203], v[74:77]
	v_mfma_f32_16x16x32_f16 v[78:81], v[30:33], v[200:203], v[78:81]
	s_waitcnt lgkmcnt(0)
	v_mfma_f32_16x16x32_f16 v[82:85], v[18:21], v[204:207], v[82:85]
	v_mfma_f32_16x16x32_f16 v[86:89], v[22:25], v[204:207], v[86:89]
	v_mfma_f32_16x16x32_f16 v[90:93], v[26:29], v[204:207], v[90:93]
	v_mfma_f32_16x16x32_f16 v[94:97], v[30:33], v[204:207], v[94:97]
	s_setprio 0
	v_add_u32_e32 v192, 0x10000, v208
	v_add_u32_e32 v196, 0x14000, v208
	v_add_u32_e32 v200, 0x18000, v208
	v_add_u32_e32 v204, 0x1c000, v208
	ds_read_b128 v[192:195], v192
	ds_read_b128 v[196:199], v196
	ds_read_b128 v[200:203], v200
	ds_read_b128 v[204:207], v204
	s_setprio 1
	s_waitcnt lgkmcnt(3)
	v_mfma_f32_16x16x32_f16 v[98:101], v[18:21], v[192:195], v[98:101]
	v_mfma_f32_16x16x32_f16 v[102:105], v[22:25], v[192:195], v[102:105]
	v_mfma_f32_16x16x32_f16 v[106:109], v[26:29], v[192:195], v[106:109]
	v_mfma_f32_16x16x32_f16 v[110:113], v[30:33], v[192:195], v[110:113]
	s_waitcnt lgkmcnt(2)
	v_mfma_f32_16x16x32_f16 v[114:117], v[18:21], v[196:199], v[114:117]
	v_mfma_f32_16x16x32_f16 v[118:121], v[22:25], v[196:199], v[118:121]
	v_mfma_f32_16x16x32_f16 v[122:125], v[26:29], v[196:199], v[122:125]
	v_mfma_f32_16x16x32_f16 v[126:129], v[30:33], v[196:199], v[126:129]
	s_waitcnt lgkmcnt(1)
	v_mfma_f32_16x16x32_f16 v[130:133], v[18:21], v[200:203], v[130:133]
	v_mfma_f32_16x16x32_f16 v[134:137], v[22:25], v[200:203], v[134:137]
	v_mfma_f32_16x16x32_f16 v[138:141], v[26:29], v[200:203], v[138:141]
	s_waitcnt lgkmcnt(0)
	v_mfma_f32_16x16x32_f16 v[2:5], v[18:21], v[204:207], v[2:5]
	v_mfma_f32_16x16x32_f16 v[6:9], v[22:25], v[204:207], v[6:9]
	v_mfma_f32_16x16x32_f16 v[10:13], v[26:29], v[204:207], v[10:13]
	v_mfma_f32_16x16x32_f16 v[14:17], v[30:33], v[204:207], v[14:17]
	v_mfma_f32_16x16x32_f16 v[142:145], v[30:33], v[200:203], v[142:145]
	s_setprio 0
	s_xor_b32 s7, s51, 4
	s_lshl_b32 s0, s7, 12
	v_lshl_add_u64 v[30:31], v[166:167], 0, s[0:1]
	global_load_dwordx4 v[18:21], v[30:31], off
	global_load_dwordx4 v[22:25], v[30:31], off offset:1024
	global_load_dwordx4 v[26:29], v[30:31], off offset:2048
	s_nop 0
	global_load_dwordx4 v[30:33], v[30:31], off offset:3072
	v_lshl_add_u32 v208, s2, 10, v191
	ds_read_b128 v[192:195], v208
	ds_read_b128 v[196:199], v208 offset:16384
	ds_read_b128 v[200:203], v208 offset:32768
	ds_read_b128 v[204:207], v208 offset:49152
	s_setprio 1
	s_waitcnt vmcnt(11) lgkmcnt(3)
	v_mfma_f32_16x16x32_f16 v[34:37], v[162:165], v[192:195], v[34:37]
	s_waitcnt vmcnt(10)
	v_mfma_f32_16x16x32_f16 v[38:41], v[168:171], v[192:195], v[38:41]
	s_waitcnt vmcnt(9)
	v_mfma_f32_16x16x32_f16 v[42:45], v[172:175], v[192:195], v[42:45]
	s_waitcnt vmcnt(8)
	v_mfma_f32_16x16x32_f16 v[46:49], v[176:179], v[192:195], v[46:49]
	s_waitcnt lgkmcnt(2)
	v_mfma_f32_16x16x32_f16 v[50:53], v[162:165], v[196:199], v[50:53]
	v_mfma_f32_16x16x32_f16 v[54:57], v[168:171], v[196:199], v[54:57]
	v_mfma_f32_16x16x32_f16 v[58:61], v[172:175], v[196:199], v[58:61]
	v_mfma_f32_16x16x32_f16 v[62:65], v[176:179], v[196:199], v[62:65]
	s_waitcnt lgkmcnt(1)
	v_mfma_f32_16x16x32_f16 v[66:69], v[162:165], v[200:203], v[66:69]
	v_mfma_f32_16x16x32_f16 v[70:73], v[168:171], v[200:203], v[70:73]
	v_mfma_f32_16x16x32_f16 v[74:77], v[172:175], v[200:203], v[74:77]
	v_mfma_f32_16x16x32_f16 v[78:81], v[176:179], v[200:203], v[78:81]
	s_waitcnt lgkmcnt(0)
	v_mfma_f32_16x16x32_f16 v[82:85], v[162:165], v[204:207], v[82:85]
	v_mfma_f32_16x16x32_f16 v[86:89], v[168:171], v[204:207], v[86:89]
	v_mfma_f32_16x16x32_f16 v[90:93], v[172:175], v[204:207], v[90:93]
	v_mfma_f32_16x16x32_f16 v[94:97], v[176:179], v[204:207], v[94:97]
	s_setprio 0
	v_add_u32_e32 v192, 0x10000, v208
	v_add_u32_e32 v196, 0x14000, v208
	v_add_u32_e32 v200, 0x18000, v208
	v_add_u32_e32 v204, 0x1c000, v208
	ds_read_b128 v[192:195], v192
	ds_read_b128 v[196:199], v196
	ds_read_b128 v[200:203], v200
	ds_read_b128 v[204:207], v204
	s_setprio 1
	s_waitcnt lgkmcnt(3)
	v_mfma_f32_16x16x32_f16 v[98:101], v[162:165], v[192:195], v[98:101]
	v_mfma_f32_16x16x32_f16 v[102:105], v[168:171], v[192:195], v[102:105]
	v_mfma_f32_16x16x32_f16 v[106:109], v[172:175], v[192:195], v[106:109]
	v_mfma_f32_16x16x32_f16 v[110:113], v[176:179], v[192:195], v[110:113]
	s_waitcnt lgkmcnt(2)
	v_mfma_f32_16x16x32_f16 v[114:117], v[162:165], v[196:199], v[114:117]
	v_mfma_f32_16x16x32_f16 v[118:121], v[168:171], v[196:199], v[118:121]
	v_mfma_f32_16x16x32_f16 v[122:125], v[172:175], v[196:199], v[122:125]
	v_mfma_f32_16x16x32_f16 v[126:129], v[176:179], v[196:199], v[126:129]
	s_waitcnt lgkmcnt(1)
	v_mfma_f32_16x16x32_f16 v[130:133], v[162:165], v[200:203], v[130:133]
	v_mfma_f32_16x16x32_f16 v[134:137], v[168:171], v[200:203], v[134:137]
	v_mfma_f32_16x16x32_f16 v[138:141], v[172:175], v[200:203], v[138:141]
	s_waitcnt lgkmcnt(0)
	v_mfma_f32_16x16x32_f16 v[2:5], v[162:165], v[204:207], v[2:5]
	v_mfma_f32_16x16x32_f16 v[6:9], v[168:171], v[204:207], v[6:9]
	v_mfma_f32_16x16x32_f16 v[10:13], v[172:175], v[204:207], v[10:13]
	v_mfma_f32_16x16x32_f16 v[14:17], v[176:179], v[204:207], v[14:17]
	v_mfma_f32_16x16x32_f16 v[142:145], v[176:179], v[200:203], v[142:145]
	s_setprio 0
	s_or_b32 s2, s49, s30
	s_lshl_b32 s0, s2, 12
	v_lshl_add_u64 v[176:177], v[166:167], 0, s[0:1]
	global_load_dwordx4 v[162:165], v[176:177], off
	global_load_dwordx4 v[168:171], v[176:177], off offset:1024
	global_load_dwordx4 v[172:175], v[176:177], off offset:2048
	s_nop 0
	global_load_dwordx4 v[176:179], v[176:177], off offset:3072
	v_lshl_add_u32 v208, s3, 10, v191
	ds_read_b128 v[192:195], v208
	ds_read_b128 v[196:199], v208 offset:16384
	ds_read_b128 v[200:203], v208 offset:32768
	ds_read_b128 v[204:207], v208 offset:49152
	s_setprio 1
	s_waitcnt vmcnt(11) lgkmcnt(3)
	v_mfma_f32_16x16x32_f16 v[34:37], v[146:149], v[192:195], v[34:37]
	s_waitcnt vmcnt(10)
	v_mfma_f32_16x16x32_f16 v[38:41], v[150:153], v[192:195], v[38:41]
	s_waitcnt vmcnt(9)
	v_mfma_f32_16x16x32_f16 v[42:45], v[154:157], v[192:195], v[42:45]
	s_waitcnt vmcnt(8)
	v_mfma_f32_16x16x32_f16 v[46:49], v[158:161], v[192:195], v[46:49]
	s_waitcnt lgkmcnt(2)
	v_mfma_f32_16x16x32_f16 v[50:53], v[146:149], v[196:199], v[50:53]
	v_mfma_f32_16x16x32_f16 v[54:57], v[150:153], v[196:199], v[54:57]
	v_mfma_f32_16x16x32_f16 v[58:61], v[154:157], v[196:199], v[58:61]
	v_mfma_f32_16x16x32_f16 v[62:65], v[158:161], v[196:199], v[62:65]
	s_waitcnt lgkmcnt(1)
	v_mfma_f32_16x16x32_f16 v[66:69], v[146:149], v[200:203], v[66:69]
	v_mfma_f32_16x16x32_f16 v[70:73], v[150:153], v[200:203], v[70:73]
	v_mfma_f32_16x16x32_f16 v[74:77], v[154:157], v[200:203], v[74:77]
	v_mfma_f32_16x16x32_f16 v[78:81], v[158:161], v[200:203], v[78:81]
	s_waitcnt lgkmcnt(0)
	v_mfma_f32_16x16x32_f16 v[82:85], v[146:149], v[204:207], v[82:85]
	v_mfma_f32_16x16x32_f16 v[86:89], v[150:153], v[204:207], v[86:89]
	v_mfma_f32_16x16x32_f16 v[90:93], v[154:157], v[204:207], v[90:93]
	v_mfma_f32_16x16x32_f16 v[94:97], v[158:161], v[204:207], v[94:97]
	s_setprio 0
	v_add_u32_e32 v192, 0x10000, v208
	v_add_u32_e32 v196, 0x14000, v208
	v_add_u32_e32 v200, 0x18000, v208
	v_add_u32_e32 v204, 0x1c000, v208
	ds_read_b128 v[192:195], v192
	ds_read_b128 v[196:199], v196
	ds_read_b128 v[200:203], v200
	ds_read_b128 v[204:207], v204
	s_setprio 1
	s_waitcnt lgkmcnt(3)
	v_mfma_f32_16x16x32_f16 v[98:101], v[146:149], v[192:195], v[98:101]
	v_mfma_f32_16x16x32_f16 v[102:105], v[150:153], v[192:195], v[102:105]
	v_mfma_f32_16x16x32_f16 v[106:109], v[154:157], v[192:195], v[106:109]
	v_mfma_f32_16x16x32_f16 v[110:113], v[158:161], v[192:195], v[110:113]
	s_waitcnt lgkmcnt(2)
	v_mfma_f32_16x16x32_f16 v[114:117], v[146:149], v[196:199], v[114:117]
	v_mfma_f32_16x16x32_f16 v[118:121], v[150:153], v[196:199], v[118:121]
	v_mfma_f32_16x16x32_f16 v[122:125], v[154:157], v[196:199], v[122:125]
	v_mfma_f32_16x16x32_f16 v[126:129], v[158:161], v[196:199], v[126:129]
	s_waitcnt lgkmcnt(1)
	v_mfma_f32_16x16x32_f16 v[130:133], v[146:149], v[200:203], v[130:133]
	v_mfma_f32_16x16x32_f16 v[134:137], v[150:153], v[200:203], v[134:137]
	v_mfma_f32_16x16x32_f16 v[138:141], v[154:157], v[200:203], v[138:141]
	s_waitcnt lgkmcnt(0)
	v_mfma_f32_16x16x32_f16 v[2:5], v[146:149], v[204:207], v[2:5]
	v_mfma_f32_16x16x32_f16 v[6:9], v[150:153], v[204:207], v[6:9]
	v_mfma_f32_16x16x32_f16 v[10:13], v[154:157], v[204:207], v[10:13]
	v_mfma_f32_16x16x32_f16 v[14:17], v[158:161], v[204:207], v[14:17]
	v_mfma_f32_16x16x32_f16 v[142:145], v[158:161], v[200:203], v[142:145]
	s_setprio 0
	s_or_b32 s3, s49, s31
	s_lshl_b32 s0, s3, 12
	v_lshl_add_u64 v[158:159], v[166:167], 0, s[0:1]
	global_load_dwordx4 v[146:149], v[158:159], off
	global_load_dwordx4 v[150:153], v[158:159], off offset:1024
	global_load_dwordx4 v[154:157], v[158:159], off offset:2048
	s_nop 0
	global_load_dwordx4 v[158:161], v[158:159], off offset:3072
	v_lshl_add_u32 v208, s7, 10, v191
	ds_read_b128 v[192:195], v208
	ds_read_b128 v[196:199], v208 offset:16384
	ds_read_b128 v[200:203], v208 offset:32768
	ds_read_b128 v[204:207], v208 offset:49152
	s_setprio 1
	s_waitcnt vmcnt(11) lgkmcnt(3)
	v_mfma_f32_16x16x32_f16 v[34:37], v[18:21], v[192:195], v[34:37]
	s_waitcnt vmcnt(10)
	v_mfma_f32_16x16x32_f16 v[38:41], v[22:25], v[192:195], v[38:41]
	s_waitcnt vmcnt(9)
	v_mfma_f32_16x16x32_f16 v[42:45], v[26:29], v[192:195], v[42:45]
	s_waitcnt vmcnt(8)
	v_mfma_f32_16x16x32_f16 v[46:49], v[30:33], v[192:195], v[46:49]
	s_waitcnt lgkmcnt(2)
	v_mfma_f32_16x16x32_f16 v[50:53], v[18:21], v[196:199], v[50:53]
	v_mfma_f32_16x16x32_f16 v[54:57], v[22:25], v[196:199], v[54:57]
	v_mfma_f32_16x16x32_f16 v[58:61], v[26:29], v[196:199], v[58:61]
	v_mfma_f32_16x16x32_f16 v[62:65], v[30:33], v[196:199], v[62:65]
	s_waitcnt lgkmcnt(1)
	v_mfma_f32_16x16x32_f16 v[66:69], v[18:21], v[200:203], v[66:69]
	v_mfma_f32_16x16x32_f16 v[70:73], v[22:25], v[200:203], v[70:73]
	v_mfma_f32_16x16x32_f16 v[74:77], v[26:29], v[200:203], v[74:77]
	v_mfma_f32_16x16x32_f16 v[78:81], v[30:33], v[200:203], v[78:81]
	s_waitcnt lgkmcnt(0)
	v_mfma_f32_16x16x32_f16 v[82:85], v[18:21], v[204:207], v[82:85]
	v_mfma_f32_16x16x32_f16 v[86:89], v[22:25], v[204:207], v[86:89]
	v_mfma_f32_16x16x32_f16 v[90:93], v[26:29], v[204:207], v[90:93]
	v_mfma_f32_16x16x32_f16 v[94:97], v[30:33], v[204:207], v[94:97]
	s_setprio 0
	v_add_u32_e32 v192, 0x10000, v208
	v_add_u32_e32 v196, 0x14000, v208
	v_add_u32_e32 v200, 0x18000, v208
	v_add_u32_e32 v204, 0x1c000, v208
	ds_read_b128 v[192:195], v192
	ds_read_b128 v[196:199], v196
	ds_read_b128 v[200:203], v200
	ds_read_b128 v[204:207], v204
	s_setprio 1
	s_waitcnt lgkmcnt(3)
	v_mfma_f32_16x16x32_f16 v[98:101], v[18:21], v[192:195], v[98:101]
	v_mfma_f32_16x16x32_f16 v[102:105], v[22:25], v[192:195], v[102:105]
	v_mfma_f32_16x16x32_f16 v[106:109], v[26:29], v[192:195], v[106:109]
	v_mfma_f32_16x16x32_f16 v[110:113], v[30:33], v[192:195], v[110:113]
	s_waitcnt lgkmcnt(2)
	v_mfma_f32_16x16x32_f16 v[114:117], v[18:21], v[196:199], v[114:117]
	v_mfma_f32_16x16x32_f16 v[118:121], v[22:25], v[196:199], v[118:121]
	v_mfma_f32_16x16x32_f16 v[122:125], v[26:29], v[196:199], v[122:125]
	v_mfma_f32_16x16x32_f16 v[126:129], v[30:33], v[196:199], v[126:129]
	s_waitcnt lgkmcnt(1)
	v_mfma_f32_16x16x32_f16 v[130:133], v[18:21], v[200:203], v[130:133]
	v_mfma_f32_16x16x32_f16 v[134:137], v[22:25], v[200:203], v[134:137]
	v_mfma_f32_16x16x32_f16 v[138:141], v[26:29], v[200:203], v[138:141]
	s_waitcnt lgkmcnt(0)
	v_mfma_f32_16x16x32_f16 v[2:5], v[18:21], v[204:207], v[2:5]
	v_mfma_f32_16x16x32_f16 v[6:9], v[22:25], v[204:207], v[6:9]
	v_mfma_f32_16x16x32_f16 v[10:13], v[26:29], v[204:207], v[10:13]
	v_mfma_f32_16x16x32_f16 v[14:17], v[30:33], v[204:207], v[14:17]
	v_mfma_f32_16x16x32_f16 v[142:145], v[30:33], v[200:203], v[142:145]
	s_setprio 0
	s_or_b32 s7, s49, s48
	s_lshl_b32 s0, s7, 12
	v_lshl_add_u64 v[26:27], v[166:167], 0, s[0:1]
	global_load_dwordx4 v[18:21], v[26:27], off
	global_load_dwordx4 v[22:25], v[26:27], off offset:1024
	global_load_dwordx4 v[30:33], v[26:27], off offset:2048
	global_load_dwordx4 v[192:195], v[26:27], off offset:3072
	v_lshl_add_u32 v166, s2, 10, v191
	ds_read_b128 v[26:29], v166
	ds_read_b128 v[196:199], v166 offset:16384
	ds_read_b128 v[200:203], v166 offset:32768
	ds_read_b128 v[204:207], v166 offset:49152
	s_setprio 1
	s_waitcnt vmcnt(11) lgkmcnt(3)
	v_mfma_f32_16x16x32_f16 v[34:37], v[162:165], v[26:29], v[34:37]
	s_waitcnt vmcnt(10)
	v_mfma_f32_16x16x32_f16 v[38:41], v[168:171], v[26:29], v[38:41]
	s_waitcnt vmcnt(9)
	v_mfma_f32_16x16x32_f16 v[42:45], v[172:175], v[26:29], v[42:45]
	s_waitcnt vmcnt(8)
	v_mfma_f32_16x16x32_f16 v[26:29], v[176:179], v[26:29], v[46:49]
	s_waitcnt lgkmcnt(2)
	v_mfma_f32_16x16x32_f16 v[46:49], v[162:165], v[196:199], v[50:53]
	v_mfma_f32_16x16x32_f16 v[50:53], v[168:171], v[196:199], v[54:57]
	v_mfma_f32_16x16x32_f16 v[54:57], v[172:175], v[196:199], v[58:61]
	v_mfma_f32_16x16x32_f16 v[58:61], v[176:179], v[196:199], v[62:65]
	s_waitcnt lgkmcnt(1)
	v_mfma_f32_16x16x32_f16 v[62:65], v[162:165], v[200:203], v[66:69]
	v_mfma_f32_16x16x32_f16 v[66:69], v[168:171], v[200:203], v[70:73]
	v_mfma_f32_16x16x32_f16 v[70:73], v[172:175], v[200:203], v[74:77]
	v_mfma_f32_16x16x32_f16 v[74:77], v[176:179], v[200:203], v[78:81]
	s_waitcnt lgkmcnt(0)
	v_mfma_f32_16x16x32_f16 v[78:81], v[162:165], v[204:207], v[82:85]
	v_mfma_f32_16x16x32_f16 v[82:85], v[168:171], v[204:207], v[86:89]
	v_mfma_f32_16x16x32_f16 v[86:89], v[172:175], v[204:207], v[90:93]
	v_mfma_f32_16x16x32_f16 v[90:93], v[176:179], v[204:207], v[94:97]
	s_setprio 0
	s_nop 1
	v_add_u32_e32 v94, 0x10000, v166
	v_add_u32_e32 v167, 0x14000, v166
	ds_read_b128 v[94:97], v94
	ds_read_b128 v[196:199], v167
	v_add_u32_e32 v167, 0x18000, v166
	v_add_u32_e32 v166, 0x1c000, v166
	ds_read_b128 v[200:203], v167
	ds_read_b128 v[204:207], v166
	s_setprio 1
	s_waitcnt lgkmcnt(3)
	v_mfma_f32_16x16x32_f16 v[98:101], v[162:165], v[94:97], v[98:101]
	v_mfma_f32_16x16x32_f16 v[102:105], v[168:171], v[94:97], v[102:105]
	v_mfma_f32_16x16x32_f16 v[106:109], v[172:175], v[94:97], v[106:109]
	v_mfma_f32_16x16x32_f16 v[94:97], v[176:179], v[94:97], v[110:113]
	s_waitcnt lgkmcnt(2)
	v_mfma_f32_16x16x32_f16 v[110:113], v[162:165], v[196:199], v[114:117]
	v_mfma_f32_16x16x32_f16 v[114:117], v[168:171], v[196:199], v[118:121]
	v_mfma_f32_16x16x32_f16 v[118:121], v[172:175], v[196:199], v[122:125]
	v_mfma_f32_16x16x32_f16 v[122:125], v[176:179], v[196:199], v[126:129]
	s_waitcnt lgkmcnt(1)
	v_mfma_f32_16x16x32_f16 v[126:129], v[162:165], v[200:203], v[130:133]
	v_mfma_f32_16x16x32_f16 v[130:133], v[168:171], v[200:203], v[134:137]
	v_mfma_f32_16x16x32_f16 v[134:137], v[172:175], v[200:203], v[138:141]
	v_mfma_f32_16x16x32_f16 v[138:141], v[176:179], v[200:203], v[142:145]
	s_waitcnt lgkmcnt(0)
	v_mfma_f32_16x16x32_f16 v[2:5], v[162:165], v[204:207], v[2:5]
	v_mfma_f32_16x16x32_f16 v[6:9], v[168:171], v[204:207], v[6:9]
	v_mfma_f32_16x16x32_f16 v[10:13], v[172:175], v[204:207], v[10:13]
	v_mfma_f32_16x16x32_f16 v[14:17], v[176:179], v[204:207], v[14:17]
	s_setprio 0
	v_lshl_add_u32 v174, s3, 10, v191
	ds_read_b128 v[142:145], v174
	ds_read_b128 v[162:165], v174 offset:16384
	ds_read_b128 v[166:169], v174 offset:32768
	ds_read_b128 v[170:173], v174 offset:49152
	s_setprio 1
	s_waitcnt vmcnt(7) lgkmcnt(3)
	v_mfma_f32_16x16x32_f16 v[34:37], v[146:149], v[142:145], v[34:37]
	s_waitcnt vmcnt(6)
	v_mfma_f32_16x16x32_f16 v[38:41], v[150:153], v[142:145], v[38:41]
	s_waitcnt vmcnt(5)
	v_mfma_f32_16x16x32_f16 v[42:45], v[154:157], v[142:145], v[42:45]
	s_waitcnt vmcnt(4)
	v_mfma_f32_16x16x32_f16 v[26:29], v[158:161], v[142:145], v[26:29]
	s_waitcnt lgkmcnt(2)
	v_mfma_f32_16x16x32_f16 v[46:49], v[146:149], v[162:165], v[46:49]
	v_mfma_f32_16x16x32_f16 v[50:53], v[150:153], v[162:165], v[50:53]
	v_mfma_f32_16x16x32_f16 v[54:57], v[154:157], v[162:165], v[54:57]
	v_mfma_f32_16x16x32_f16 v[58:61], v[158:161], v[162:165], v[58:61]
	s_waitcnt lgkmcnt(1)
	v_mfma_f32_16x16x32_f16 v[62:65], v[146:149], v[166:169], v[62:65]
	v_mfma_f32_16x16x32_f16 v[66:69], v[150:153], v[166:169], v[66:69]
	v_mfma_f32_16x16x32_f16 v[70:73], v[154:157], v[166:169], v[70:73]
	v_mfma_f32_16x16x32_f16 v[74:77], v[158:161], v[166:169], v[74:77]
	s_waitcnt lgkmcnt(0)
	v_mfma_f32_16x16x32_f16 v[78:81], v[146:149], v[170:173], v[78:81]
	v_mfma_f32_16x16x32_f16 v[82:85], v[150:153], v[170:173], v[82:85]
	v_mfma_f32_16x16x32_f16 v[86:89], v[154:157], v[170:173], v[86:89]
	v_mfma_f32_16x16x32_f16 v[162:165], v[158:161], v[170:173], v[90:93]
	s_setprio 0
	s_nop 1
	v_add_u32_e32 v90, 0x10000, v174
	v_add_u32_e32 v142, 0x14000, v174
	v_add_u32_e32 v166, 0x18000, v174
	v_add_u32_e32 v170, 0x1c000, v174
	ds_read_b128 v[90:93], v90
	ds_read_b128 v[142:145], v142
	ds_read_b128 v[166:169], v166
	ds_read_b128 v[170:173], v170
	s_setprio 1
	s_waitcnt lgkmcnt(0)
	v_mfma_f32_16x16x32_f16 v[2:5], v[146:149], v[170:173], v[2:5]
	v_mfma_f32_16x16x32_f16 v[6:9], v[150:153], v[170:173], v[6:9]
	v_mfma_f32_16x16x32_f16 v[10:13], v[154:157], v[170:173], v[10:13]
	v_mfma_f32_16x16x32_f16 v[14:17], v[158:161], v[170:173], v[14:17]
	v_mfma_f32_16x16x32_f16 v[174:177], v[146:149], v[90:93], v[98:101]
	v_mfma_f32_16x16x32_f16 v[196:199], v[150:153], v[90:93], v[102:105]
	v_mfma_f32_16x16x32_f16 v[200:203], v[154:157], v[90:93], v[106:109]
	v_mfma_f32_16x16x32_f16 v[204:207], v[158:161], v[90:93], v[94:97]
	v_mfma_f32_16x16x32_f16 v[208:211], v[146:149], v[142:145], v[110:113]
	v_mfma_f32_16x16x32_f16 v[212:215], v[150:153], v[142:145], v[114:117]
	v_mfma_f32_16x16x32_f16 v[216:219], v[154:157], v[142:145], v[118:121]
	v_mfma_f32_16x16x32_f16 v[220:223], v[158:161], v[142:145], v[122:125]
	v_mfma_f32_16x16x32_f16 v[224:227], v[146:149], v[166:169], v[126:129]
	v_mfma_f32_16x16x32_f16 v[228:231], v[150:153], v[166:169], v[130:133]
	v_mfma_f32_16x16x32_f16 v[232:235], v[154:157], v[166:169], v[134:137]
	v_mfma_f32_16x16x32_f16 v[166:169], v[158:161], v[166:169], v[138:141]
	s_setprio 0
	v_lshl_add_u32 v158, s7, 10, v191
	ds_read_b128 v[90:93], v158
	ds_read_b128 v[94:97], v158 offset:16384
	ds_read_b128 v[98:101], v158 offset:32768
	ds_read_b128 v[146:149], v158 offset:49152
	s_setprio 1
	s_waitcnt vmcnt(3) lgkmcnt(3)
	v_mfma_f32_16x16x32_f16 v[150:153], v[18:21], v[90:93], v[34:37]
	s_waitcnt vmcnt(2)
	v_mfma_f32_16x16x32_f16 v[138:141], v[22:25], v[90:93], v[38:41]
	s_waitcnt vmcnt(1)
	v_mfma_f32_16x16x32_f16 v[154:157], v[30:33], v[90:93], v[42:45]
	s_waitcnt vmcnt(0)
	v_mfma_f32_16x16x32_f16 v[142:145], v[192:195], v[90:93], v[26:29]
	s_waitcnt lgkmcnt(2)
	v_mfma_f32_16x16x32_f16 v[134:137], v[18:21], v[94:97], v[46:49]
	v_mfma_f32_16x16x32_f16 v[122:125], v[22:25], v[94:97], v[50:53]
	v_mfma_f32_16x16x32_f16 v[130:133], v[30:33], v[94:97], v[54:57]
	v_mfma_f32_16x16x32_f16 v[126:129], v[192:195], v[94:97], v[58:61]
	s_waitcnt lgkmcnt(1)
	v_mfma_f32_16x16x32_f16 v[118:121], v[18:21], v[98:101], v[62:65]
	v_mfma_f32_16x16x32_f16 v[106:109], v[22:25], v[98:101], v[66:69]
	v_mfma_f32_16x16x32_f16 v[114:117], v[30:33], v[98:101], v[70:73]
	v_mfma_f32_16x16x32_f16 v[110:113], v[192:195], v[98:101], v[74:77]
	s_waitcnt lgkmcnt(0)
	v_mfma_f32_16x16x32_f16 v[102:105], v[18:21], v[146:149], v[78:81]
	v_mfma_f32_16x16x32_f16 v[90:93], v[22:25], v[146:149], v[82:85]
	v_mfma_f32_16x16x32_f16 v[98:101], v[30:33], v[146:149], v[86:89]
	v_mfma_f32_16x16x32_f16 v[94:97], v[192:195], v[146:149], v[162:165]
	s_setprio 0
	v_add_u32_e32 v26, 0x10000, v158
	v_add_u32_e32 v34, 0x14000, v158
	v_add_u32_e32 v38, 0x18000, v158
	ds_read_b128 v[26:29], v26
	ds_read_b128 v[34:37], v34
	v_add_u32_e32 v42, 0x1c000, v158
	ds_read_b128 v[38:41], v38
	ds_read_b128 v[146:149], v42
	s_setprio 1
	s_waitcnt lgkmcnt(3)
	v_mfma_f32_16x16x32_f16 v[86:89], v[18:21], v[26:29], v[174:177]
	v_mfma_f32_16x16x32_f16 v[74:77], v[22:25], v[26:29], v[196:199]
	v_mfma_f32_16x16x32_f16 v[82:85], v[30:33], v[26:29], v[200:203]
	v_mfma_f32_16x16x32_f16 v[78:81], v[192:195], v[26:29], v[204:207]
	s_waitcnt lgkmcnt(2)
	v_mfma_f32_16x16x32_f16 v[70:73], v[18:21], v[34:37], v[208:211]
	v_mfma_f32_16x16x32_f16 v[58:61], v[22:25], v[34:37], v[212:215]
	v_mfma_f32_16x16x32_f16 v[66:69], v[30:33], v[34:37], v[216:219]
	v_mfma_f32_16x16x32_f16 v[62:65], v[192:195], v[34:37], v[220:223]
	s_waitcnt lgkmcnt(1)
	v_mfma_f32_16x16x32_f16 v[54:57], v[18:21], v[38:41], v[224:227]
	v_mfma_f32_16x16x32_f16 v[42:45], v[22:25], v[38:41], v[228:231]
	v_mfma_f32_16x16x32_f16 v[50:53], v[30:33], v[38:41], v[232:235]
	v_mfma_f32_16x16x32_f16 v[46:49], v[192:195], v[38:41], v[166:169]
	s_waitcnt lgkmcnt(0)
	v_mfma_f32_16x16x32_f16 v[26:29], v[18:21], v[146:149], v[2:5]
	v_mfma_f32_16x16x32_f16 v[2:5], v[22:25], v[146:149], v[6:9]
	v_mfma_f32_16x16x32_f16 v[22:25], v[30:33], v[146:149], v[10:13]
	v_mfma_f32_16x16x32_f16 v[6:9], v[192:195], v[146:149], v[14:17]
	s_setprio 0
	s_lshl_b64 s[0:1], s[42:43], 2
	s_add_u32 s0, s18, s0
	s_addc_u32 s1, s19, s1
	s_lshl_b32 s2, s42, 8
	s_ashr_i32 s3, s2, 31
	v_lshlrev_b32_e32 v146, 5, v187
	s_lshl_b64 s[2:3], s[2:3], 2
	v_and_or_b32 v10, v190, 12, v146
	s_add_u32 s12, s12, s2
	s_addc_u32 s13, s13, s3
	v_lshlrev_b32_e32 v10, 2, v10
	v_add_u32_e32 v254, 0x22640, v10
	ds_read_b128 v[34:37], v254
	ds_read_b128 v[14:17], v254 offset:64
	ds_read_b128 v[38:41], v254 offset:1024
	ds_read_b128 v[18:21], v254 offset:1088
	ds_read_b128 v[30:33], v254 offset:2048
	ds_read_b128 v[10:13], v254 offset:2112
	s_add_u32 s12, s14, s2
	s_addc_u32 s13, s15, s3
	s_add_u32 s2, s16, s2
	s_addc_u32 s3, s17, s3
	s_nop 0
	v_cmp_gt_u32_e32 vcc, 16, v189
	s_mov_b32 s2, s69
	v_mov_b32_e32 v216, 0x3d38aa3b
	v_mov_b32_e32 v217, 0x3d38aa3b
	v_mov_b32_e32 v218, 0xbcb8aa3b
	v_mov_b32_e32 v219, 0xbcb8aa3b
	v_mov_b32_e32 v222, 1.0
	v_mov_b32_e32 v223, 1.0
	v_mov_b32_e32 v224, 0x4038aa3b
	v_mov_b32_e32 v225, 0x4038aa3b
	v_mov_b32_e32 v226, 0xbfb8aa3b
	v_mov_b32_e32 v227, 0xbfb8aa3b
	v_lshlrev_b32_e32 v232, 9, v187
	v_lshlrev_b32_e32 v233, 2, v188
	v_add3_u32 v232, s24, v232, v233
	s_waitcnt vmcnt(0) lgkmcnt(0)
	v_pk_mul_f32 v[34:35], v[34:35], v[224:225]
	v_pk_mul_f32 v[36:37], v[36:37], v[224:225]
	v_pk_mul_f32 v[14:15], v[14:15], v[224:225]
	v_pk_mul_f32 v[16:17], v[16:17], v[224:225]
	v_pk_mul_f32 v[38:39], v[38:39], v[226:227]
	v_pk_mul_f32 v[40:41], v[40:41], v[226:227]
	v_pk_mul_f32 v[18:19], v[18:19], v[226:227]
	v_pk_mul_f32 v[20:21], v[20:21], v[226:227]
	v_pk_fma_f32 v[150:151], v[150:151], v[216:217], v[34:35]
	v_pk_fma_f32 v[154:155], v[154:155], v[218:219], v[38:39]
	v_min_f32_e32 v150, 0x42700000, v150
	v_min_f32_e32 v151, 0x42700000, v151
	v_min_f32_e32 v154, 0x42700000, v154
	v_min_f32_e32 v155, 0x42700000, v155
	v_pk_fma_f32 v[152:153], v[152:153], v[216:217], v[36:37]
	v_pk_fma_f32 v[156:157], v[156:157], v[218:219], v[40:41]
	v_min_f32_e32 v152, 0x42700000, v152
	v_min_f32_e32 v153, 0x42700000, v153
	v_min_f32_e32 v156, 0x42700000, v156
	v_min_f32_e32 v157, 0x42700000, v157
	v_exp_f32_e32 v150, v150
	v_exp_f32_e32 v151, v151
	v_exp_f32_e32 v154, v154
	v_exp_f32_e32 v155, v155
	v_exp_f32_e32 v152, v152
	v_exp_f32_e32 v153, v153
	v_exp_f32_e32 v156, v156
	v_exp_f32_e32 v157, v157
	v_pk_fma_f32 v[228:229], v[150:151], v[30:31], v[30:31] neg_lo:[0,0,1] neg_hi:[0,0,1]
	v_pk_add_f32 v[154:155], v[154:155], v[222:223]
	v_pk_fma_f32 v[150:151], v[150:151], v[154:155], v[154:155]
	v_pk_fma_f32 v[230:231], v[152:153], v[32:33], v[32:33] neg_lo:[0,0,1] neg_hi:[0,0,1]
	v_pk_add_f32 v[156:157], v[156:157], v[222:223]
	v_pk_fma_f32 v[152:153], v[152:153], v[156:157], v[156:157]
	v_rcp_f32_e32 v150, v150
	v_rcp_f32_e32 v151, v151
	v_rcp_f32_e32 v152, v152
	v_rcp_f32_e32 v153, v153
	v_pk_mul_f32 v[200:201], v[228:229], v[150:151]
	v_pk_fma_f32 v[200:201], v[230:231], v[152:153], v[200:201]
	v_pk_fma_f32 v[138:139], v[138:139], v[216:217], v[14:15]
	v_pk_fma_f32 v[142:143], v[142:143], v[218:219], v[18:19]
	v_min_f32_e32 v138, 0x42700000, v138
	v_min_f32_e32 v139, 0x42700000, v139
	v_min_f32_e32 v142, 0x42700000, v142
	v_min_f32_e32 v143, 0x42700000, v143
	v_pk_fma_f32 v[140:141], v[140:141], v[216:217], v[16:17]
	v_pk_fma_f32 v[144:145], v[144:145], v[218:219], v[20:21]
	v_min_f32_e32 v140, 0x42700000, v140
	v_min_f32_e32 v141, 0x42700000, v141
	v_min_f32_e32 v144, 0x42700000, v144
	v_min_f32_e32 v145, 0x42700000, v145
	v_exp_f32_e32 v138, v138
	v_exp_f32_e32 v139, v139
	v_exp_f32_e32 v142, v142
	v_exp_f32_e32 v143, v143
	v_exp_f32_e32 v140, v140
	v_exp_f32_e32 v141, v141
	v_exp_f32_e32 v144, v144
	v_exp_f32_e32 v145, v145
	v_pk_fma_f32 v[228:229], v[138:139], v[10:11], v[10:11] neg_lo:[0,0,1] neg_hi:[0,0,1]
	v_pk_add_f32 v[142:143], v[142:143], v[222:223]
	v_pk_fma_f32 v[138:139], v[138:139], v[142:143], v[142:143]
	v_pk_fma_f32 v[230:231], v[140:141], v[12:13], v[12:13] neg_lo:[0,0,1] neg_hi:[0,0,1]
	v_pk_add_f32 v[144:145], v[144:145], v[222:223]
	v_pk_fma_f32 v[140:141], v[140:141], v[144:145], v[144:145]
	v_rcp_f32_e32 v138, v138
	v_rcp_f32_e32 v139, v139
	v_rcp_f32_e32 v140, v140
	v_rcp_f32_e32 v141, v141
	v_pk_fma_f32 v[200:201], v[228:229], v[138:139], v[200:201]
	v_pk_fma_f32 v[200:201], v[230:231], v[140:141], v[200:201]
	v_pk_fma_f32 v[134:135], v[134:135], v[216:217], v[34:35]
	v_pk_fma_f32 v[130:131], v[130:131], v[218:219], v[38:39]
	v_min_f32_e32 v134, 0x42700000, v134
	v_min_f32_e32 v135, 0x42700000, v135
	v_min_f32_e32 v130, 0x42700000, v130
	v_min_f32_e32 v131, 0x42700000, v131
	v_pk_fma_f32 v[136:137], v[136:137], v[216:217], v[36:37]
	v_pk_fma_f32 v[132:133], v[132:133], v[218:219], v[40:41]
	v_min_f32_e32 v136, 0x42700000, v136
	v_min_f32_e32 v137, 0x42700000, v137
	v_min_f32_e32 v132, 0x42700000, v132
	v_min_f32_e32 v133, 0x42700000, v133
	v_exp_f32_e32 v134, v134
	v_exp_f32_e32 v135, v135
	v_exp_f32_e32 v130, v130
	v_exp_f32_e32 v131, v131
	v_exp_f32_e32 v136, v136
	v_exp_f32_e32 v137, v137
	v_exp_f32_e32 v132, v132
	v_exp_f32_e32 v133, v133
	v_pk_fma_f32 v[228:229], v[134:135], v[30:31], v[30:31] neg_lo:[0,0,1] neg_hi:[0,0,1]
	v_pk_add_f32 v[130:131], v[130:131], v[222:223]
	v_pk_fma_f32 v[134:135], v[134:135], v[130:131], v[130:131]
	v_pk_fma_f32 v[230:231], v[136:137], v[32:33], v[32:33] neg_lo:[0,0,1] neg_hi:[0,0,1]
	v_pk_add_f32 v[132:133], v[132:133], v[222:223]
	v_pk_fma_f32 v[136:137], v[136:137], v[132:133], v[132:133]
	v_rcp_f32_e32 v134, v134
	v_rcp_f32_e32 v135, v135
	v_rcp_f32_e32 v136, v136
	v_rcp_f32_e32 v137, v137
	v_pk_mul_f32 v[202:203], v[228:229], v[134:135]
	v_pk_fma_f32 v[202:203], v[230:231], v[136:137], v[202:203]
	v_pk_fma_f32 v[122:123], v[122:123], v[216:217], v[14:15]
	v_pk_fma_f32 v[126:127], v[126:127], v[218:219], v[18:19]
	v_min_f32_e32 v122, 0x42700000, v122
	v_min_f32_e32 v123, 0x42700000, v123
	v_min_f32_e32 v126, 0x42700000, v126
	v_min_f32_e32 v127, 0x42700000, v127
	v_pk_fma_f32 v[124:125], v[124:125], v[216:217], v[16:17]
	v_pk_fma_f32 v[128:129], v[128:129], v[218:219], v[20:21]
	v_min_f32_e32 v124, 0x42700000, v124
	v_min_f32_e32 v125, 0x42700000, v125
	v_min_f32_e32 v128, 0x42700000, v128
	v_min_f32_e32 v129, 0x42700000, v129
	v_exp_f32_e32 v122, v122
	v_exp_f32_e32 v123, v123
	v_exp_f32_e32 v126, v126
	v_exp_f32_e32 v127, v127
	v_exp_f32_e32 v124, v124
	v_exp_f32_e32 v125, v125
	v_exp_f32_e32 v128, v128
	v_exp_f32_e32 v129, v129
	v_pk_fma_f32 v[228:229], v[122:123], v[10:11], v[10:11] neg_lo:[0,0,1] neg_hi:[0,0,1]
	v_pk_add_f32 v[126:127], v[126:127], v[222:223]
	v_pk_fma_f32 v[122:123], v[122:123], v[126:127], v[126:127]
	v_pk_fma_f32 v[230:231], v[124:125], v[12:13], v[12:13] neg_lo:[0,0,1] neg_hi:[0,0,1]
	v_pk_add_f32 v[128:129], v[128:129], v[222:223]
	v_pk_fma_f32 v[124:125], v[124:125], v[128:129], v[128:129]
	v_rcp_f32_e32 v122, v122
	v_rcp_f32_e32 v123, v123
	v_rcp_f32_e32 v124, v124
	v_rcp_f32_e32 v125, v125
	v_pk_fma_f32 v[202:203], v[228:229], v[122:123], v[202:203]
	v_pk_fma_f32 v[202:203], v[230:231], v[124:125], v[202:203]
	v_pk_fma_f32 v[118:119], v[118:119], v[216:217], v[34:35]
	v_pk_fma_f32 v[114:115], v[114:115], v[218:219], v[38:39]
	v_min_f32_e32 v118, 0x42700000, v118
	v_min_f32_e32 v119, 0x42700000, v119
	v_min_f32_e32 v114, 0x42700000, v114
	v_min_f32_e32 v115, 0x42700000, v115
	v_pk_fma_f32 v[120:121], v[120:121], v[216:217], v[36:37]
	v_pk_fma_f32 v[116:117], v[116:117], v[218:219], v[40:41]
	v_min_f32_e32 v120, 0x42700000, v120
	v_min_f32_e32 v121, 0x42700000, v121
	v_min_f32_e32 v116, 0x42700000, v116
	v_min_f32_e32 v117, 0x42700000, v117
	v_exp_f32_e32 v118, v118
	v_exp_f32_e32 v119, v119
	v_exp_f32_e32 v114, v114
	v_exp_f32_e32 v115, v115
	v_exp_f32_e32 v120, v120
	v_exp_f32_e32 v121, v121
	v_exp_f32_e32 v116, v116
	v_exp_f32_e32 v117, v117
	v_pk_fma_f32 v[228:229], v[118:119], v[30:31], v[30:31] neg_lo:[0,0,1] neg_hi:[0,0,1]
	v_pk_add_f32 v[114:115], v[114:115], v[222:223]
	v_pk_fma_f32 v[118:119], v[118:119], v[114:115], v[114:115]
	v_pk_fma_f32 v[230:231], v[120:121], v[32:33], v[32:33] neg_lo:[0,0,1] neg_hi:[0,0,1]
	v_pk_add_f32 v[116:117], v[116:117], v[222:223]
	v_pk_fma_f32 v[120:121], v[120:121], v[116:117], v[116:117]
	v_rcp_f32_e32 v118, v118
	v_rcp_f32_e32 v119, v119
	v_rcp_f32_e32 v120, v120
	v_rcp_f32_e32 v121, v121
	v_pk_mul_f32 v[204:205], v[228:229], v[118:119]
	v_pk_fma_f32 v[204:205], v[230:231], v[120:121], v[204:205]
	v_pk_fma_f32 v[106:107], v[106:107], v[216:217], v[14:15]
	v_pk_fma_f32 v[110:111], v[110:111], v[218:219], v[18:19]
	v_min_f32_e32 v106, 0x42700000, v106
	v_min_f32_e32 v107, 0x42700000, v107
	v_min_f32_e32 v110, 0x42700000, v110
	v_min_f32_e32 v111, 0x42700000, v111
	v_pk_fma_f32 v[108:109], v[108:109], v[216:217], v[16:17]
	v_pk_fma_f32 v[112:113], v[112:113], v[218:219], v[20:21]
	v_min_f32_e32 v108, 0x42700000, v108
	v_min_f32_e32 v109, 0x42700000, v109
	v_min_f32_e32 v112, 0x42700000, v112
	v_min_f32_e32 v113, 0x42700000, v113
	v_exp_f32_e32 v106, v106
	v_exp_f32_e32 v107, v107
	v_exp_f32_e32 v110, v110
	v_exp_f32_e32 v111, v111
	v_exp_f32_e32 v108, v108
	v_exp_f32_e32 v109, v109
	v_exp_f32_e32 v112, v112
	v_exp_f32_e32 v113, v113
	v_pk_fma_f32 v[228:229], v[106:107], v[10:11], v[10:11] neg_lo:[0,0,1] neg_hi:[0,0,1]
	v_pk_add_f32 v[110:111], v[110:111], v[222:223]
	v_pk_fma_f32 v[106:107], v[106:107], v[110:111], v[110:111]
	v_pk_fma_f32 v[230:231], v[108:109], v[12:13], v[12:13] neg_lo:[0,0,1] neg_hi:[0,0,1]
	v_pk_add_f32 v[112:113], v[112:113], v[222:223]
	v_pk_fma_f32 v[108:109], v[108:109], v[112:113], v[112:113]
	v_rcp_f32_e32 v106, v106
	v_rcp_f32_e32 v107, v107
	v_rcp_f32_e32 v108, v108
	v_rcp_f32_e32 v109, v109
	v_pk_fma_f32 v[204:205], v[228:229], v[106:107], v[204:205]
	v_pk_fma_f32 v[204:205], v[230:231], v[108:109], v[204:205]
	v_pk_fma_f32 v[102:103], v[102:103], v[216:217], v[34:35]
	v_pk_fma_f32 v[98:99], v[98:99], v[218:219], v[38:39]
	v_min_f32_e32 v102, 0x42700000, v102
	v_min_f32_e32 v103, 0x42700000, v103
	v_min_f32_e32 v98, 0x42700000, v98
	v_min_f32_e32 v99, 0x42700000, v99
	v_pk_fma_f32 v[104:105], v[104:105], v[216:217], v[36:37]
	v_pk_fma_f32 v[100:101], v[100:101], v[218:219], v[40:41]
	v_min_f32_e32 v104, 0x42700000, v104
	v_min_f32_e32 v105, 0x42700000, v105
	v_min_f32_e32 v100, 0x42700000, v100
	v_min_f32_e32 v101, 0x42700000, v101
	v_exp_f32_e32 v102, v102
	v_exp_f32_e32 v103, v103
	v_exp_f32_e32 v98, v98
	v_exp_f32_e32 v99, v99
	v_exp_f32_e32 v104, v104
	v_exp_f32_e32 v105, v105
	v_exp_f32_e32 v100, v100
	v_exp_f32_e32 v101, v101
	v_pk_fma_f32 v[228:229], v[102:103], v[30:31], v[30:31] neg_lo:[0,0,1] neg_hi:[0,0,1]
	v_pk_add_f32 v[98:99], v[98:99], v[222:223]
	v_pk_fma_f32 v[102:103], v[102:103], v[98:99], v[98:99]
	v_pk_fma_f32 v[230:231], v[104:105], v[32:33], v[32:33] neg_lo:[0,0,1] neg_hi:[0,0,1]
	v_pk_add_f32 v[100:101], v[100:101], v[222:223]
	v_pk_fma_f32 v[104:105], v[104:105], v[100:101], v[100:101]
	v_rcp_f32_e32 v102, v102
	v_rcp_f32_e32 v103, v103
	v_rcp_f32_e32 v104, v104
	v_rcp_f32_e32 v105, v105
	v_pk_mul_f32 v[206:207], v[228:229], v[102:103]
	v_pk_fma_f32 v[206:207], v[230:231], v[104:105], v[206:207]
	v_pk_fma_f32 v[90:91], v[90:91], v[216:217], v[14:15]
	v_pk_fma_f32 v[94:95], v[94:95], v[218:219], v[18:19]
	v_min_f32_e32 v90, 0x42700000, v90
	v_min_f32_e32 v91, 0x42700000, v91
	v_min_f32_e32 v94, 0x42700000, v94
	v_min_f32_e32 v95, 0x42700000, v95
	v_pk_fma_f32 v[92:93], v[92:93], v[216:217], v[16:17]
	v_pk_fma_f32 v[96:97], v[96:97], v[218:219], v[20:21]
	v_min_f32_e32 v92, 0x42700000, v92
	v_min_f32_e32 v93, 0x42700000, v93
	v_min_f32_e32 v96, 0x42700000, v96
	v_min_f32_e32 v97, 0x42700000, v97
	v_exp_f32_e32 v90, v90
	v_exp_f32_e32 v91, v91
	v_exp_f32_e32 v94, v94
	v_exp_f32_e32 v95, v95
	v_exp_f32_e32 v92, v92
	v_exp_f32_e32 v93, v93
	v_exp_f32_e32 v96, v96
	v_exp_f32_e32 v97, v97
	v_pk_fma_f32 v[228:229], v[90:91], v[10:11], v[10:11] neg_lo:[0,0,1] neg_hi:[0,0,1]
	v_pk_add_f32 v[94:95], v[94:95], v[222:223]
	v_pk_fma_f32 v[90:91], v[90:91], v[94:95], v[94:95]
	v_pk_fma_f32 v[230:231], v[92:93], v[12:13], v[12:13] neg_lo:[0,0,1] neg_hi:[0,0,1]
	v_pk_add_f32 v[96:97], v[96:97], v[222:223]
	v_pk_fma_f32 v[92:93], v[92:93], v[96:97], v[96:97]
	v_rcp_f32_e32 v90, v90
	v_rcp_f32_e32 v91, v91
	v_rcp_f32_e32 v92, v92
	v_rcp_f32_e32 v93, v93
	v_pk_fma_f32 v[206:207], v[228:229], v[90:91], v[206:207]
	v_pk_fma_f32 v[206:207], v[230:231], v[92:93], v[206:207]
	v_pk_fma_f32 v[86:87], v[86:87], v[216:217], v[34:35]
	v_pk_fma_f32 v[82:83], v[82:83], v[218:219], v[38:39]
	v_min_f32_e32 v86, 0x42700000, v86
	v_min_f32_e32 v87, 0x42700000, v87
	v_min_f32_e32 v82, 0x42700000, v82
	v_min_f32_e32 v83, 0x42700000, v83
	v_pk_fma_f32 v[88:89], v[88:89], v[216:217], v[36:37]
	v_pk_fma_f32 v[84:85], v[84:85], v[218:219], v[40:41]
	v_min_f32_e32 v88, 0x42700000, v88
	v_min_f32_e32 v89, 0x42700000, v89
	v_min_f32_e32 v84, 0x42700000, v84
	v_min_f32_e32 v85, 0x42700000, v85
	v_exp_f32_e32 v86, v86
	v_exp_f32_e32 v87, v87
	v_exp_f32_e32 v82, v82
	v_exp_f32_e32 v83, v83
	v_exp_f32_e32 v88, v88
	v_exp_f32_e32 v89, v89
	v_exp_f32_e32 v84, v84
	v_exp_f32_e32 v85, v85
	v_pk_fma_f32 v[228:229], v[86:87], v[30:31], v[30:31] neg_lo:[0,0,1] neg_hi:[0,0,1]
	v_pk_add_f32 v[82:83], v[82:83], v[222:223]
	v_pk_fma_f32 v[86:87], v[86:87], v[82:83], v[82:83]
	v_pk_fma_f32 v[230:231], v[88:89], v[32:33], v[32:33] neg_lo:[0,0,1] neg_hi:[0,0,1]
	v_pk_add_f32 v[84:85], v[84:85], v[222:223]
	v_pk_fma_f32 v[88:89], v[88:89], v[84:85], v[84:85]
	v_rcp_f32_e32 v86, v86
	v_rcp_f32_e32 v87, v87
	v_rcp_f32_e32 v88, v88
	v_rcp_f32_e32 v89, v89
	v_pk_mul_f32 v[208:209], v[228:229], v[86:87]
	v_pk_fma_f32 v[208:209], v[230:231], v[88:89], v[208:209]
	v_pk_fma_f32 v[74:75], v[74:75], v[216:217], v[14:15]
	v_pk_fma_f32 v[78:79], v[78:79], v[218:219], v[18:19]
	v_min_f32_e32 v74, 0x42700000, v74
	v_min_f32_e32 v75, 0x42700000, v75
	v_min_f32_e32 v78, 0x42700000, v78
	v_min_f32_e32 v79, 0x42700000, v79
	v_pk_fma_f32 v[76:77], v[76:77], v[216:217], v[16:17]
	v_pk_fma_f32 v[80:81], v[80:81], v[218:219], v[20:21]
	v_min_f32_e32 v76, 0x42700000, v76
	v_min_f32_e32 v77, 0x42700000, v77
	v_min_f32_e32 v80, 0x42700000, v80
	v_min_f32_e32 v81, 0x42700000, v81
	v_exp_f32_e32 v74, v74
	v_exp_f32_e32 v75, v75
	v_exp_f32_e32 v78, v78
	v_exp_f32_e32 v79, v79
	v_exp_f32_e32 v76, v76
	v_exp_f32_e32 v77, v77
	v_exp_f32_e32 v80, v80
	v_exp_f32_e32 v81, v81
	v_pk_fma_f32 v[228:229], v[74:75], v[10:11], v[10:11] neg_lo:[0,0,1] neg_hi:[0,0,1]
	v_pk_add_f32 v[78:79], v[78:79], v[222:223]
	v_pk_fma_f32 v[74:75], v[74:75], v[78:79], v[78:79]
	v_pk_fma_f32 v[230:231], v[76:77], v[12:13], v[12:13] neg_lo:[0,0,1] neg_hi:[0,0,1]
	v_pk_add_f32 v[80:81], v[80:81], v[222:223]
	v_pk_fma_f32 v[76:77], v[76:77], v[80:81], v[80:81]
	v_rcp_f32_e32 v74, v74
	v_rcp_f32_e32 v75, v75
	v_rcp_f32_e32 v76, v76
	v_rcp_f32_e32 v77, v77
	v_pk_fma_f32 v[208:209], v[228:229], v[74:75], v[208:209]
	v_pk_fma_f32 v[208:209], v[230:231], v[76:77], v[208:209]
	v_pk_fma_f32 v[70:71], v[70:71], v[216:217], v[34:35]
	v_pk_fma_f32 v[66:67], v[66:67], v[218:219], v[38:39]
	v_min_f32_e32 v70, 0x42700000, v70
	v_min_f32_e32 v71, 0x42700000, v71
	v_min_f32_e32 v66, 0x42700000, v66
	v_min_f32_e32 v67, 0x42700000, v67
	v_pk_fma_f32 v[72:73], v[72:73], v[216:217], v[36:37]
	v_pk_fma_f32 v[68:69], v[68:69], v[218:219], v[40:41]
	v_min_f32_e32 v72, 0x42700000, v72
	v_min_f32_e32 v73, 0x42700000, v73
	v_min_f32_e32 v68, 0x42700000, v68
	v_min_f32_e32 v69, 0x42700000, v69
	v_exp_f32_e32 v70, v70
	v_exp_f32_e32 v71, v71
	v_exp_f32_e32 v66, v66
	v_exp_f32_e32 v67, v67
	v_exp_f32_e32 v72, v72
	v_exp_f32_e32 v73, v73
	v_exp_f32_e32 v68, v68
	v_exp_f32_e32 v69, v69
	v_pk_fma_f32 v[228:229], v[70:71], v[30:31], v[30:31] neg_lo:[0,0,1] neg_hi:[0,0,1]
	v_pk_add_f32 v[66:67], v[66:67], v[222:223]
	v_pk_fma_f32 v[70:71], v[70:71], v[66:67], v[66:67]
	v_pk_fma_f32 v[230:231], v[72:73], v[32:33], v[32:33] neg_lo:[0,0,1] neg_hi:[0,0,1]
	v_pk_add_f32 v[68:69], v[68:69], v[222:223]
	v_pk_fma_f32 v[72:73], v[72:73], v[68:69], v[68:69]
	v_rcp_f32_e32 v70, v70
	v_rcp_f32_e32 v71, v71
	v_rcp_f32_e32 v72, v72
	v_rcp_f32_e32 v73, v73
	v_pk_mul_f32 v[210:211], v[228:229], v[70:71]
	v_pk_fma_f32 v[210:211], v[230:231], v[72:73], v[210:211]
	v_pk_fma_f32 v[58:59], v[58:59], v[216:217], v[14:15]
	v_pk_fma_f32 v[62:63], v[62:63], v[218:219], v[18:19]
	v_min_f32_e32 v58, 0x42700000, v58
	v_min_f32_e32 v59, 0x42700000, v59
	v_min_f32_e32 v62, 0x42700000, v62
	v_min_f32_e32 v63, 0x42700000, v63
	v_pk_fma_f32 v[60:61], v[60:61], v[216:217], v[16:17]
	v_pk_fma_f32 v[64:65], v[64:65], v[218:219], v[20:21]
	v_min_f32_e32 v60, 0x42700000, v60
	v_min_f32_e32 v61, 0x42700000, v61
	v_min_f32_e32 v64, 0x42700000, v64
	v_min_f32_e32 v65, 0x42700000, v65
	v_exp_f32_e32 v58, v58
	v_exp_f32_e32 v59, v59
	v_exp_f32_e32 v62, v62
	v_exp_f32_e32 v63, v63
	v_exp_f32_e32 v60, v60
	v_exp_f32_e32 v61, v61
	v_exp_f32_e32 v64, v64
	v_exp_f32_e32 v65, v65
	v_pk_fma_f32 v[228:229], v[58:59], v[10:11], v[10:11] neg_lo:[0,0,1] neg_hi:[0,0,1]
	v_pk_add_f32 v[62:63], v[62:63], v[222:223]
	v_pk_fma_f32 v[58:59], v[58:59], v[62:63], v[62:63]
	v_pk_fma_f32 v[230:231], v[60:61], v[12:13], v[12:13] neg_lo:[0,0,1] neg_hi:[0,0,1]
	v_pk_add_f32 v[64:65], v[64:65], v[222:223]
	v_pk_fma_f32 v[60:61], v[60:61], v[64:65], v[64:65]
	v_rcp_f32_e32 v58, v58
	v_rcp_f32_e32 v59, v59
	v_rcp_f32_e32 v60, v60
	v_rcp_f32_e32 v61, v61
	v_pk_fma_f32 v[210:211], v[228:229], v[58:59], v[210:211]
	v_pk_fma_f32 v[210:211], v[230:231], v[60:61], v[210:211]
	v_pk_fma_f32 v[54:55], v[54:55], v[216:217], v[34:35]
	v_pk_fma_f32 v[50:51], v[50:51], v[218:219], v[38:39]
	v_min_f32_e32 v54, 0x42700000, v54
	v_min_f32_e32 v55, 0x42700000, v55
	v_min_f32_e32 v50, 0x42700000, v50
	v_min_f32_e32 v51, 0x42700000, v51
	v_pk_fma_f32 v[56:57], v[56:57], v[216:217], v[36:37]
	v_pk_fma_f32 v[52:53], v[52:53], v[218:219], v[40:41]
	v_min_f32_e32 v56, 0x42700000, v56
	v_min_f32_e32 v57, 0x42700000, v57
	v_min_f32_e32 v52, 0x42700000, v52
	v_min_f32_e32 v53, 0x42700000, v53
	v_exp_f32_e32 v54, v54
	v_exp_f32_e32 v55, v55
	v_exp_f32_e32 v50, v50
	v_exp_f32_e32 v51, v51
	v_exp_f32_e32 v56, v56
	v_exp_f32_e32 v57, v57
	v_exp_f32_e32 v52, v52
	v_exp_f32_e32 v53, v53
	v_pk_fma_f32 v[228:229], v[54:55], v[30:31], v[30:31] neg_lo:[0,0,1] neg_hi:[0,0,1]
	v_pk_add_f32 v[50:51], v[50:51], v[222:223]
	v_pk_fma_f32 v[54:55], v[54:55], v[50:51], v[50:51]
	v_pk_fma_f32 v[230:231], v[56:57], v[32:33], v[32:33] neg_lo:[0,0,1] neg_hi:[0,0,1]
	v_pk_add_f32 v[52:53], v[52:53], v[222:223]
	v_pk_fma_f32 v[56:57], v[56:57], v[52:53], v[52:53]
	v_rcp_f32_e32 v54, v54
	v_rcp_f32_e32 v55, v55
	v_rcp_f32_e32 v56, v56
	v_rcp_f32_e32 v57, v57
	v_pk_mul_f32 v[212:213], v[228:229], v[54:55]
	v_pk_fma_f32 v[212:213], v[230:231], v[56:57], v[212:213]
	v_pk_fma_f32 v[42:43], v[42:43], v[216:217], v[14:15]
	v_pk_fma_f32 v[46:47], v[46:47], v[218:219], v[18:19]
	v_min_f32_e32 v42, 0x42700000, v42
	v_min_f32_e32 v43, 0x42700000, v43
	v_min_f32_e32 v46, 0x42700000, v46
	v_min_f32_e32 v47, 0x42700000, v47
	v_pk_fma_f32 v[44:45], v[44:45], v[216:217], v[16:17]
	v_pk_fma_f32 v[48:49], v[48:49], v[218:219], v[20:21]
	v_min_f32_e32 v44, 0x42700000, v44
	v_min_f32_e32 v45, 0x42700000, v45
	v_min_f32_e32 v48, 0x42700000, v48
	v_min_f32_e32 v49, 0x42700000, v49
	v_exp_f32_e32 v42, v42
	v_exp_f32_e32 v43, v43
	v_exp_f32_e32 v46, v46
	v_exp_f32_e32 v47, v47
	v_exp_f32_e32 v44, v44
	v_exp_f32_e32 v45, v45
	v_exp_f32_e32 v48, v48
	v_exp_f32_e32 v49, v49
	v_pk_fma_f32 v[228:229], v[42:43], v[10:11], v[10:11] neg_lo:[0,0,1] neg_hi:[0,0,1]
	v_pk_add_f32 v[46:47], v[46:47], v[222:223]
	v_pk_fma_f32 v[42:43], v[42:43], v[46:47], v[46:47]
	v_pk_fma_f32 v[230:231], v[44:45], v[12:13], v[12:13] neg_lo:[0,0,1] neg_hi:[0,0,1]
	v_pk_add_f32 v[48:49], v[48:49], v[222:223]
	v_pk_fma_f32 v[44:45], v[44:45], v[48:49], v[48:49]
	v_rcp_f32_e32 v42, v42
	v_rcp_f32_e32 v43, v43
	v_rcp_f32_e32 v44, v44
	v_rcp_f32_e32 v45, v45
	v_pk_fma_f32 v[212:213], v[228:229], v[42:43], v[212:213]
	v_pk_fma_f32 v[212:213], v[230:231], v[44:45], v[212:213]
	v_pk_fma_f32 v[26:27], v[26:27], v[216:217], v[34:35]
	v_pk_fma_f32 v[22:23], v[22:23], v[218:219], v[38:39]
	v_min_f32_e32 v26, 0x42700000, v26
	v_min_f32_e32 v27, 0x42700000, v27
	v_min_f32_e32 v22, 0x42700000, v22
	v_min_f32_e32 v23, 0x42700000, v23
	v_pk_fma_f32 v[28:29], v[28:29], v[216:217], v[36:37]
	v_pk_fma_f32 v[24:25], v[24:25], v[218:219], v[40:41]
	v_min_f32_e32 v28, 0x42700000, v28
	v_min_f32_e32 v29, 0x42700000, v29
	v_min_f32_e32 v24, 0x42700000, v24
	v_min_f32_e32 v25, 0x42700000, v25
	v_exp_f32_e32 v26, v26
	v_exp_f32_e32 v27, v27
	v_exp_f32_e32 v22, v22
	v_exp_f32_e32 v23, v23
	v_exp_f32_e32 v28, v28
	v_exp_f32_e32 v29, v29
	v_exp_f32_e32 v24, v24
	v_exp_f32_e32 v25, v25
	v_pk_fma_f32 v[228:229], v[26:27], v[30:31], v[30:31] neg_lo:[0,0,1] neg_hi:[0,0,1]
	v_pk_add_f32 v[22:23], v[22:23], v[222:223]
	v_pk_fma_f32 v[26:27], v[26:27], v[22:23], v[22:23]
	v_pk_fma_f32 v[230:231], v[28:29], v[32:33], v[32:33] neg_lo:[0,0,1] neg_hi:[0,0,1]
	v_pk_add_f32 v[24:25], v[24:25], v[222:223]
	v_pk_fma_f32 v[28:29], v[28:29], v[24:25], v[24:25]
	v_rcp_f32_e32 v26, v26
	v_rcp_f32_e32 v27, v27
	v_rcp_f32_e32 v28, v28
	v_rcp_f32_e32 v29, v29
	v_pk_mul_f32 v[214:215], v[228:229], v[26:27]
	v_pk_fma_f32 v[214:215], v[230:231], v[28:29], v[214:215]
	v_pk_fma_f32 v[2:3], v[2:3], v[216:217], v[14:15]
	v_pk_fma_f32 v[6:7], v[6:7], v[218:219], v[18:19]
	v_min_f32_e32 v2, 0x42700000, v2
	v_min_f32_e32 v3, 0x42700000, v3
	v_min_f32_e32 v6, 0x42700000, v6
	v_min_f32_e32 v7, 0x42700000, v7
	v_pk_fma_f32 v[4:5], v[4:5], v[216:217], v[16:17]
	v_pk_fma_f32 v[8:9], v[8:9], v[218:219], v[20:21]
	v_min_f32_e32 v4, 0x42700000, v4
	v_min_f32_e32 v5, 0x42700000, v5
	v_min_f32_e32 v8, 0x42700000, v8
	v_min_f32_e32 v9, 0x42700000, v9
	v_exp_f32_e32 v2, v2
	v_exp_f32_e32 v3, v3
	v_exp_f32_e32 v6, v6
	v_exp_f32_e32 v7, v7
	v_exp_f32_e32 v4, v4
	v_exp_f32_e32 v5, v5
	v_exp_f32_e32 v8, v8
	v_exp_f32_e32 v9, v9
	v_pk_fma_f32 v[228:229], v[2:3], v[10:11], v[10:11] neg_lo:[0,0,1] neg_hi:[0,0,1]
	v_pk_add_f32 v[6:7], v[6:7], v[222:223]
	v_pk_fma_f32 v[2:3], v[2:3], v[6:7], v[6:7]
	v_pk_fma_f32 v[230:231], v[4:5], v[12:13], v[12:13] neg_lo:[0,0,1] neg_hi:[0,0,1]
	v_pk_add_f32 v[8:9], v[8:9], v[222:223]
	v_pk_fma_f32 v[4:5], v[4:5], v[8:9], v[8:9]
	v_rcp_f32_e32 v2, v2
	v_rcp_f32_e32 v3, v3
	v_rcp_f32_e32 v4, v4
	v_rcp_f32_e32 v5, v5
	v_pk_fma_f32 v[214:215], v[228:229], v[2:3], v[214:215]
	v_pk_fma_f32 v[214:215], v[230:231], v[4:5], v[214:215]
	v_add_f32_e32 v240, v200, v201
	v_add_f32_e32 v241, v202, v203
	v_add_f32_e32 v242, v204, v205
	v_add_f32_e32 v243, v206, v207
	v_add_f32_e32 v244, v208, v209
	v_add_f32_e32 v245, v210, v211
	v_add_f32_e32 v246, v212, v213
	v_add_f32_e32 v247, v214, v215
	ds_bpermute_b32 v200, v181, v240
	ds_bpermute_b32 v201, v181, v241
	ds_bpermute_b32 v202, v181, v242
	ds_bpermute_b32 v203, v181, v243
	ds_bpermute_b32 v204, v181, v244
	ds_bpermute_b32 v205, v181, v245
	ds_bpermute_b32 v206, v181, v246
	ds_bpermute_b32 v207, v181, v247
	s_waitcnt lgkmcnt(0)
	v_add_f32_e32 v240, v240, v200
	v_add_f32_e32 v241, v241, v201
	v_add_f32_e32 v242, v242, v202
	v_add_f32_e32 v243, v243, v203
	v_add_f32_e32 v244, v244, v204
	v_add_f32_e32 v245, v245, v205
	v_add_f32_e32 v246, v246, v206
	v_add_f32_e32 v247, v247, v207
	ds_bpermute_b32 v200, v183, v240
	ds_bpermute_b32 v201, v183, v241
	ds_bpermute_b32 v202, v183, v242
	ds_bpermute_b32 v203, v183, v243
	ds_bpermute_b32 v204, v183, v244
	ds_bpermute_b32 v205, v183, v245
	ds_bpermute_b32 v206, v183, v246
	ds_bpermute_b32 v207, v183, v247
	s_waitcnt lgkmcnt(0)
	v_add_f32_e32 v240, v240, v200
	v_add_f32_e32 v241, v241, v201
	v_add_f32_e32 v242, v242, v202
	v_add_f32_e32 v243, v243, v203
	v_add_f32_e32 v244, v244, v204
	v_add_f32_e32 v245, v245, v205
	v_add_f32_e32 v246, v246, v206
	v_add_f32_e32 v247, v247, v207
	s_and_saveexec_b64 s[64:65], vcc
	ds_write2_b32 v232, v240, v241 offset0:0 offset1:16
	ds_write2_b32 v232, v242, v243 offset0:32 offset1:48
	ds_write2_b32 v232, v244, v245 offset0:64 offset1:80
	ds_write2_b32 v232, v246, v247 offset0:96 offset1:112
	s_mov_b64 exec, s[64:65]
	v_mov_b32_e32 v4, 0
	v_lshlrev_b32_e32 v10, 2, v189
	v_mov_b32_e32 v11, v4
	v_and_b32_e32 v70, 0x1c0, v0
	s_waitcnt lgkmcnt(0)
	s_lshl_b64 s[0:1], s[42:43], 17
	s_add_u32 s96, s44, s0
	s_addc_u32 s97, s45, s1
	v_and_b32_e32 v2, 15, v0
	v_lshrrev_b32_e32 v3, 4, v0
	v_lshlrev_b32_e32 v2, 4, v2
	v_lshl_add_u32 v2, v3, 12, v2
	global_load_dwordx4 v[190:193], v2, s[96:97]
	global_load_dwordx4 v[194:197], v2, s[96:97] offset:256
	global_load_dwordx4 v[198:201], v2, s[96:97] offset:512
	global_load_dwordx4 v[202:205], v2, s[96:97] offset:768
	global_load_dwordx4 v[206:209], v2, s[96:97] offset:1024
	global_load_dwordx4 v[210:213], v2, s[96:97] offset:1280
	global_load_dwordx4 v[214:217], v2, s[96:97] offset:1536
	global_load_dwordx4 v[218:221], v2, s[96:97] offset:1792
	global_load_dwordx4 v[222:225], v2, s[96:97] offset:2048
	global_load_dwordx4 v[226:229], v2, s[96:97] offset:2304
	global_load_dwordx4 v[230:233], v2, s[96:97] offset:2560
	global_load_dwordx4 v[234:237], v2, s[96:97] offset:2816
	global_load_dwordx4 v[238:241], v2, s[96:97] offset:3072
	global_load_dwordx4 v[242:245], v2, s[96:97] offset:3328
	global_load_dwordx4 v[246:249], v2, s[96:97] offset:3584
	global_load_dwordx4 v[250:253], v2, s[96:97] offset:3840
	v_lshl_add_u32 v2, v189, 2, 0
	v_add_u32_e32 v5, 0x20000, v2
	s_waitcnt vmcnt(63) expcnt(7) lgkmcnt(15)
	s_barrier
	ds_read2st64_b32 v[2:3], v5 offset1:1
	ds_read2st64_b32 v[6:7], v5 offset0:2 offset1:3
	ds_read2st64_b32 v[8:9], v5 offset0:4 offset1:5
	ds_read2st64_b32 v[80:81], v5 offset0:6 offset1:7
	s_mov_b32 s7, 0
	s_waitcnt lgkmcnt(3)
	v_add_f32_e32 v2, s2, v2
	v_add_f32_e32 v3, s2, v3
	s_waitcnt lgkmcnt(2)
	v_add_f32_e32 v2, v2, v6
	v_add_f32_e32 v3, v3, v7
	s_waitcnt lgkmcnt(1)
	v_add_f32_e32 v2, v2, v8
	v_add_f32_e32 v6, v3, v9
	s_waitcnt lgkmcnt(0)
	v_add_f32_e32 v12, v2, v80
	ds_read2st64_b32 v[2:3], v5 offset0:8 offset1:9
	v_add_f32_e32 v14, v6, v81
	ds_read2st64_b32 v[6:7], v5 offset0:10 offset1:11
	ds_read2st64_b32 v[8:9], v5 offset0:12 offset1:13
	ds_read2st64_b32 v[80:81], v5 offset0:14 offset1:15
	v_cmp_gt_u32_e64 s[0:1], 64, v0
	s_waitcnt lgkmcnt(3)
	v_add_f32_e32 v2, v12, v2
	v_add_f32_e32 v3, v14, v3
	s_waitcnt lgkmcnt(2)
	v_add_f32_e32 v2, v2, v6
	v_add_f32_e32 v3, v3, v7
	s_waitcnt lgkmcnt(1)
	v_add_f32_e32 v2, v2, v8
	v_add_f32_e32 v3, v3, v9
	s_waitcnt lgkmcnt(0)
	v_add_f32_e32 v2, v2, v80
	v_add_f32_e32 v3, v3, v81
	v_max_f32_e32 v5, v2, v3
	s_nop 1
	v_max_f32_dpp v5, v5, v5 quad_perm:[1,0,3,2] row_mask:0xf bank_mask:0xf
	s_nop 1
	v_max_f32_dpp v5, v5, v5 quad_perm:[2,3,0,1] row_mask:0xf bank_mask:0xf
	s_nop 1
	v_max_f32_dpp v5, v5, v5 row_half_mirror row_mask:0xf bank_mask:0xf
	s_nop 1
	v_max_f32_dpp v5, v5, v5 row_mirror row_mask:0xf bank_mask:0xf
	ds_bpermute_b32 v6, v181, v5
	s_waitcnt lgkmcnt(0)
	v_max_f32_e32 v5, v5, v6
	ds_bpermute_b32 v6, v183, v5
	s_waitcnt lgkmcnt(0)
	v_max_f32_e32 v14, v5, v6
	v_sub_f32_e32 v2, v2, v14
	v_sub_f32_e32 v3, v3, v14
	v_mul_f32_e32 v2, 0x3fb8aa3b, v2
	v_mul_f32_e32 v3, 0x3fb8aa3b, v3
	v_exp_f32_e32 v2, v2
	v_exp_f32_e32 v3, v3
	s_nop 0
	v_add_f32_e32 v5, v2, v3
	s_nop 1
	v_add_f32_dpp v5, v5, v5 quad_perm:[1,0,3,2] row_mask:0xf bank_mask:0xf
	s_nop 1
	v_add_f32_dpp v5, v5, v5 quad_perm:[2,3,0,1] row_mask:0xf bank_mask:0xf
	s_nop 1
	v_add_f32_dpp v5, v5, v5 row_half_mirror row_mask:0xf bank_mask:0xf
	s_nop 1
	v_add_f32_dpp v5, v5, v5 row_mirror row_mask:0xf bank_mask:0xf
	ds_bpermute_b32 v6, v181, v5
	s_waitcnt lgkmcnt(0)
	v_add_f32_e32 v37, v5, v6
	ds_bpermute_b32 v38, v183, v37
	s_and_saveexec_b64 s[2:3], s[0:1]
	s_cbranch_execz .LBB5_166
	s_add_i32 s12, 0, 0x21000
	v_lshl_add_u32 v5, v189, 2, s12
	v_lshl_add_u32 v6, v0, 2, s12
	ds_write_b32 v5, v2
	ds_write_b32 v6, v3 offset:256

.LBB5_167:
	v_and_b32_e32 v83, 15, v12
	v_add_u32_e32 v84, s7, v82
	v_add_u32_e32 v85, 1, v12
	v_add_u32_e32 v86, 2, v12
	v_add_u32_e32 v87, 3, v12
	v_lshl_or_b32 v88, v83, 6, v186
	v_and_b32_e32 v89, 32, v84
	v_and_b32_e32 v85, 15, v85
	v_add_u32_e32 v90, 4, v84
	v_and_b32_e32 v86, 15, v86
	v_add_u32_e32 v91, 8, v84
	v_and_b32_e32 v87, 15, v87
	v_add_u32_e32 v84, 12, v84
	v_xad_u32 v88, v88, v89, v80
	v_lshl_add_u32 v83, v83, 2, v81
	v_lshl_or_b32 v89, v85, 6, v186
	v_lshl_add_u32 v92, v85, 2, v81
	v_lshl_or_b32 v93, v86, 6, v186
	v_lshl_add_u32 v96, v86, 2, v81
	v_lshl_or_b32 v94, v87, 6, v186
	v_and_b32_e32 v95, 32, v84
	v_lshl_add_u32 v101, v87, 2, v81
	ds_read_b128 v[84:87], v88
	ds_read_b32 v100, v83
	v_and_b32_e32 v90, 32, v90
	v_and_b32_e32 v91, 32, v91
	v_xad_u32 v83, v89, v90, v80
	v_xad_u32 v93, v93, v91, v80
	v_xad_u32 v97, v94, v95, v80
	ds_read_b128 v[88:91], v83
	ds_read_b32 v102, v92
	ds_read_b128 v[92:95], v93
	ds_read_b32 v104, v96
	ds_read_b128 v[96:99], v97
	ds_read_b32 v106, v101
	s_waitcnt lgkmcnt(7)
	v_cvt_f32_f16_e32 v108, v84
	v_cvt_f32_f16_sdwa v109, v84 dst_sel:DWORD dst_unused:UNUSED_PAD src0_sel:WORD_1
	v_cvt_f32_f16_e32 v84, v85
	v_cvt_f32_f16_sdwa v85, v85 dst_sel:DWORD dst_unused:UNUSED_PAD src0_sel:WORD_1
	v_cvt_f32_f16_e32 v110, v86
	v_cvt_f32_f16_sdwa v111, v86 dst_sel:DWORD dst_unused:UNUSED_PAD src0_sel:WORD_1
	v_cvt_f32_f16_e32 v86, v87
	v_cvt_f32_f16_sdwa v87, v87 dst_sel:DWORD dst_unused:UNUSED_PAD src0_sel:WORD_1
	s_waitcnt lgkmcnt(5)
	v_cvt_f32_f16_e32 v112, v88
	v_cvt_f32_f16_sdwa v113, v88 dst_sel:DWORD dst_unused:UNUSED_PAD src0_sel:WORD_1
	v_cvt_f32_f16_e32 v88, v89
	v_cvt_f32_f16_sdwa v89, v89 dst_sel:DWORD dst_unused:UNUSED_PAD src0_sel:WORD_1
	v_cvt_f32_f16_e32 v114, v90
	v_cvt_f32_f16_sdwa v115, v90 dst_sel:DWORD dst_unused:UNUSED_PAD src0_sel:WORD_1
	v_cvt_f32_f16_e32 v90, v91
	v_cvt_f32_f16_sdwa v91, v91 dst_sel:DWORD dst_unused:UNUSED_PAD src0_sel:WORD_1
	s_waitcnt lgkmcnt(3)
	v_cvt_f32_f16_e32 v116, v92
	v_cvt_f32_f16_sdwa v117, v92 dst_sel:DWORD dst_unused:UNUSED_PAD src0_sel:WORD_1
	v_cvt_f32_f16_e32 v92, v93
	v_cvt_f32_f16_sdwa v93, v93 dst_sel:DWORD dst_unused:UNUSED_PAD src0_sel:WORD_1
	v_cvt_f32_f16_e32 v118, v94
	v_cvt_f32_f16_sdwa v119, v94 dst_sel:DWORD dst_unused:UNUSED_PAD src0_sel:WORD_1
	v_cvt_f32_f16_e32 v94, v95
	v_cvt_f32_f16_sdwa v95, v95 dst_sel:DWORD dst_unused:UNUSED_PAD src0_sel:WORD_1
	s_waitcnt lgkmcnt(1)
	v_cvt_f32_f16_e32 v120, v96
	v_cvt_f32_f16_sdwa v121, v96 dst_sel:DWORD dst_unused:UNUSED_PAD src0_sel:WORD_1
	v_cvt_f32_f16_e32 v96, v97
	v_cvt_f32_f16_sdwa v97, v97 dst_sel:DWORD dst_unused:UNUSED_PAD src0_sel:WORD_1
	v_cvt_f32_f16_e32 v122, v98
	v_cvt_f32_f16_sdwa v123, v98 dst_sel:DWORD dst_unused:UNUSED_PAD src0_sel:WORD_1
	v_cvt_f32_f16_e32 v98, v99
	v_cvt_f32_f16_sdwa v99, v99 dst_sel:DWORD dst_unused:UNUSED_PAD src0_sel:WORD_1
	v_pk_fma_f32 v[6:7], v[100:101], v[108:109], v[6:7] op_sel_hi:[0,1,1]
	v_pk_fma_f32 v[8:9], v[100:101], v[84:85], v[8:9] op_sel_hi:[0,1,1]
	v_pk_fma_f32 v[2:3], v[100:101], v[110:111], v[2:3] op_sel_hi:[0,1,1]
	v_pk_fma_f32 v[4:5], v[100:101], v[86:87], v[4:5] op_sel_hi:[0,1,1]
	v_pk_fma_f32 v[6:7], v[102:103], v[112:113], v[6:7] op_sel_hi:[0,1,1]
	v_pk_fma_f32 v[8:9], v[102:103], v[88:89], v[8:9] op_sel_hi:[0,1,1]
	v_pk_fma_f32 v[2:3], v[102:103], v[114:115], v[2:3] op_sel_hi:[0,1,1]
	v_pk_fma_f32 v[4:5], v[102:103], v[90:91], v[4:5] op_sel_hi:[0,1,1]
	s_add_i32 s7, s7, 16
	v_pk_fma_f32 v[6:7], v[104:105], v[116:117], v[6:7] op_sel_hi:[0,1,1]
	v_pk_fma_f32 v[8:9], v[104:105], v[92:93], v[8:9] op_sel_hi:[0,1,1]
	v_pk_fma_f32 v[2:3], v[104:105], v[118:119], v[2:3] op_sel_hi:[0,1,1]
	v_pk_fma_f32 v[4:5], v[104:105], v[94:95], v[4:5] op_sel_hi:[0,1,1]
	v_add_u32_e32 v12, 4, v12
	s_cmp_eq_u32 s7, 64
	s_waitcnt lgkmcnt(0)
	v_pk_fma_f32 v[6:7], v[106:107], v[120:121], v[6:7] op_sel_hi:[0,1,1]
	v_pk_fma_f32 v[8:9], v[106:107], v[96:97], v[8:9] op_sel_hi:[0,1,1]
	v_pk_fma_f32 v[2:3], v[106:107], v[122:123], v[2:3] op_sel_hi:[0,1,1]
	v_pk_fma_f32 v[4:5], v[106:107], v[98:99], v[4:5] op_sel_hi:[0,1,1]
	s_cbranch_scc0 .LBB5_167
	v_lshlrev_b32_e32 v80, 11, v187
	s_add_i32 s2, 0, 0x22240
	v_lshlrev_b32_e32 v12, 5, v189
	v_add3_u32 v80, s2, v80, v12
	ds_write_b128 v80, v[6:9]
	ds_write_b128 v80, v[2:5] offset:16
	v_add_u32_e32 v8, s2, v185
	s_waitcnt lgkmcnt(0)
	s_barrier
	ds_read2st64_b32 v[2:3], v8 offset1:8
	ds_read2st64_b32 v[4:5], v8 offset0:16 offset1:24
	ds_read2st64_b32 v[6:7], v8 offset0:32 offset1:40
	s_add_i32 s2, 0, 0x21200
	v_lshl_add_u32 v70, v70, 2, s2
	s_waitcnt lgkmcnt(2)
	v_add_f32_e32 v2, 0, v2
	v_add_f32_e32 v9, v2, v3
	ds_read2st64_b32 v[2:3], v8 offset0:48 offset1:56
	s_waitcnt lgkmcnt(2)
	v_add_f32_e32 v4, v9, v4
	v_add_f32_e32 v4, v4, v5
	s_waitcnt lgkmcnt(1)
	v_add_f32_e32 v4, v4, v6
	v_add_f32_e32 v4, v4, v7
	s_waitcnt lgkmcnt(0)
	v_add_f32_e32 v2, v4, v2
	v_add_f32_e32 v2, v2, v3
	v_add_u32_e32 v3, s2, v185
	ds_write_b32 v3, v2
	s_waitcnt lgkmcnt(0)
	s_barrier
	v_bfe_u32 v88, v0, 4, 2
	v_lshl_add_u32 v88, v88, 6, v70
	ds_read_b128 v[2:5], v88
	ds_read_b128 v[6:9], v88 offset:16
	ds_read_b128 v[80:83], v88 offset:32
	ds_read_b128 v[84:87], v88 offset:48
	s_waitcnt vmcnt(0) lgkmcnt(0)
	v_pk_mul_f32 v[88:89], v[2:3], v[190:191] op_sel_hi:[0,1]
	v_pk_mul_f32 v[90:91], v[2:3], v[192:193] op_sel_hi:[0,1]
	v_pk_fma_f32 v[88:89], v[2:3], v[194:195], v[88:89] op_sel:[1,0,0] op_sel_hi:[1,1,1]
	v_pk_fma_f32 v[90:91], v[2:3], v[196:197], v[90:91] op_sel:[1,0,0] op_sel_hi:[1,1,1]
	v_pk_fma_f32 v[88:89], v[4:5], v[198:199], v[88:89] op_sel_hi:[0,1,1]
	v_pk_fma_f32 v[90:91], v[4:5], v[200:201], v[90:91] op_sel_hi:[0,1,1]
	v_pk_fma_f32 v[88:89], v[4:5], v[202:203], v[88:89] op_sel:[1,0,0] op_sel_hi:[1,1,1]
	v_pk_fma_f32 v[90:91], v[4:5], v[204:205], v[90:91] op_sel:[1,0,0] op_sel_hi:[1,1,1]
	v_pk_fma_f32 v[88:89], v[6:7], v[206:207], v[88:89] op_sel_hi:[0,1,1]
	v_pk_fma_f32 v[90:91], v[6:7], v[208:209], v[90:91] op_sel_hi:[0,1,1]
	v_pk_fma_f32 v[88:89], v[6:7], v[210:211], v[88:89] op_sel:[1,0,0] op_sel_hi:[1,1,1]
	v_pk_fma_f32 v[90:91], v[6:7], v[212:213], v[90:91] op_sel:[1,0,0] op_sel_hi:[1,1,1]
	v_pk_fma_f32 v[88:89], v[8:9], v[214:215], v[88:89] op_sel_hi:[0,1,1]
	v_pk_fma_f32 v[90:91], v[8:9], v[216:217], v[90:91] op_sel_hi:[0,1,1]
	v_pk_fma_f32 v[88:89], v[8:9], v[218:219], v[88:89] op_sel:[1,0,0] op_sel_hi:[1,1,1]
	v_pk_fma_f32 v[90:91], v[8:9], v[220:221], v[90:91] op_sel:[1,0,0] op_sel_hi:[1,1,1]
	v_pk_fma_f32 v[88:89], v[80:81], v[222:223], v[88:89] op_sel_hi:[0,1,1]
	v_pk_fma_f32 v[90:91], v[80:81], v[224:225], v[90:91] op_sel_hi:[0,1,1]
	v_pk_fma_f32 v[88:89], v[80:81], v[226:227], v[88:89] op_sel:[1,0,0] op_sel_hi:[1,1,1]
	v_pk_fma_f32 v[90:91], v[80:81], v[228:229], v[90:91] op_sel:[1,0,0] op_sel_hi:[1,1,1]
	v_pk_fma_f32 v[88:89], v[82:83], v[230:231], v[88:89] op_sel_hi:[0,1,1]
	v_pk_fma_f32 v[90:91], v[82:83], v[232:233], v[90:91] op_sel_hi:[0,1,1]
	v_pk_fma_f32 v[88:89], v[82:83], v[234:235], v[88:89] op_sel:[1,0,0] op_sel_hi:[1,1,1]
	v_pk_fma_f32 v[90:91], v[82:83], v[236:237], v[90:91] op_sel:[1,0,0] op_sel_hi:[1,1,1]
	v_pk_fma_f32 v[88:89], v[84:85], v[238:239], v[88:89] op_sel_hi:[0,1,1]
	v_pk_fma_f32 v[90:91], v[84:85], v[240:241], v[90:91] op_sel_hi:[0,1,1]
	v_pk_fma_f32 v[88:89], v[84:85], v[242:243], v[88:89] op_sel:[1,0,0] op_sel_hi:[1,1,1]
	v_pk_fma_f32 v[90:91], v[84:85], v[244:245], v[90:91] op_sel:[1,0,0] op_sel_hi:[1,1,1]
	v_pk_fma_f32 v[88:89], v[86:87], v[246:247], v[88:89] op_sel_hi:[0,1,1]
	v_pk_fma_f32 v[90:91], v[86:87], v[248:249], v[90:91] op_sel_hi:[0,1,1]
	v_pk_fma_f32 v[88:89], v[86:87], v[250:251], v[88:89] op_sel:[1,0,0] op_sel_hi:[1,1,1]
	v_pk_fma_f32 v[90:91], v[86:87], v[252:253], v[90:91] op_sel:[1,0,0] op_sel_hi:[1,1,1]
	ds_bpermute_b32 v92, v181, v88
	ds_bpermute_b32 v93, v181, v89
	ds_bpermute_b32 v94, v181, v90
	ds_bpermute_b32 v95, v181, v91
	s_waitcnt lgkmcnt(0)
	v_pk_add_f32 v[88:89], v[88:89], v[92:93]
	v_pk_add_f32 v[90:91], v[90:91], v[94:95]
	ds_bpermute_b32 v92, v183, v88
	ds_bpermute_b32 v93, v183, v89
	ds_bpermute_b32 v94, v183, v90
	ds_bpermute_b32 v95, v183, v91
	s_waitcnt lgkmcnt(0)
	v_pk_add_f32 v[88:89], v[88:89], v[92:93]
	v_pk_add_f32 v[90:91], v[90:91], v[94:95]
	v_and_b32_e32 v92, 15, v0
	v_lshlrev_b32_e32 v92, 4, v92
	v_lshrrev_b32_e32 v93, 6, v0
	v_lshl_add_u32 v92, v93, 8, v92
	v_add_u32_e32 v92, 0x20000, v92
	v_cmp_gt_u32_e32 vcc, 16, v189
	s_and_saveexec_b64 s[96:97], vcc
	ds_write_b128 v92, v[88:91]
	s_mov_b64 exec, s[96:97]
	v_add_u32_e32 v2, 0, v185
	v_add_u32_e32 v2, 0x20000, v2
	s_waitcnt lgkmcnt(0)
	s_barrier
	s_and_saveexec_b64 s[2:3], s[0:1]
	s_cbranch_execz .LBB5_170
	ds_read2st64_b32 v[4:5], v2 offset1:1
	ds_read2st64_b32 v[6:7], v2 offset0:2 offset1:3
	ds_read2st64_b32 v[8:9], v2 offset0:4 offset1:5
	ds_read2st64_b32 v[2:3], v2 offset0:6 offset1:7
	s_lshl_b64 s[12:13], s[34:35], 11
	s_waitcnt lgkmcnt(3)
	v_add_f32_e32 v4, 0, v4
	v_add_f32_e32 v4, v4, v5
	s_waitcnt lgkmcnt(2)
	v_add_f32_e32 v4, v4, v6
	v_add_f32_e32 v4, v4, v7
	s_waitcnt lgkmcnt(1)
	v_add_f32_e32 v4, v4, v8
	s_add_u32 s7, s20, s12
	v_add_f32_e32 v4, v4, v9
	s_addc_u32 s13, s21, s13
	s_lshl_b32 s12, s33, 8
	s_waitcnt lgkmcnt(0)
	v_add_f32_e32 v2, v4, v2
	s_add_u32 s12, s7, s12
	v_add_f32_e32 v2, v2, v3
	s_addc_u32 s13, s13, 0
	global_store_dword v185, v2, s[12:13] sc1
